# v13 + fp8 MFMA: v_mfma_f32_16x16x128_f8f6f4 (fp8 e4m3 operands, implicit unit scales) instead of the _scale_ form with explicit 1.0 scales; bit-identical math
# speedup vs baseline: 1.0043x; 1.0002x over previous
; #define PG8_STAGE(bufoff, rs_, soff_, voff) do { _Pragma("unroll") for (int _i = 0; _i < 2; ++_i) \
;         __builtin_amdgcn_raw_ptr_buffer_load_lds(rs_, (LAS void*)(lds + (bufoff) + ldsw + _i * 8192), 16, (int)(voff)[_i], (int)(soff_), 0, 0); } while (0)
; #define PG8_LDA(dst, b, h) do { _Pragma("unroll") for (int m = 0; m < 4; ++m) dst[m] = PG8_LD2(lds + PG8_SA(b, h) + aoff + m * 2048); } while (0)
; #define PG8_LDB(dst, b, h) do { _Pragma("unroll") for (int n = 0; n < 2; ++n) dst[n] = PG8_LD2(lds + PG8_SB(b, h) + boff + n * 2048); } while (0)
; #define PG8_WAIT_V(n) asm volatile("s_waitcnt vmcnt(" #n ")" ::: "memory")
; #define PG8_WAIT_L(n) asm volatile("s_waitcnt lgkmcnt(" #n ")" ::: "memory")
; #define PG8_BAR __builtin_amdgcn_s_barrier()
; #define PG8_SCHED __builtin_amdgcn_sched_barrier(0)
; template <class Epi, class Sched, bool ALIGN_EPI = false, bool SP2 = false, bool FP8 = false>
; __device__ __forceinline__ void gemm_phase(LAS unsigned char* lds, const Gemm g, const Sched& S, const Epi& E, int wbase) {
;     ...
;             PG8_LDB(B0, 0, 0); PG8_LDB(B1, 0, 1); PG8_SCHED; PG8_LDA(At, 0, 0); PG8_STAGE(PG8_SA(1, 1), rAc, a1 + hstep, voffA);
;             PG8_WAIT_V(8); PG8_WAIT_L(0); PG8_BAR; PG8_MMA(0, 0, At, B0); PG8_MMA(0, 1, At, B1); PG8_BAR; PG8_SCHED;
;             PG8_LDA(At, 0, 1); PG8_STAGE(PG8_SB(0, 0), rB2, b2, voffB); PG8_STAGE(PG8_SB(0, 1), rB2, b2 + hstep, voffB); PG8_STAGE(PG8_SA(0, 0), rA2, a2, voffA);
;             PG8_WAIT_V(8); PG8_WAIT_L(0); PG8_BAR; PG8_MMA(1, 0, At, B0); PG8_MMA(1, 1, At, B1); PG8_BAR; PG8_SCHED;
;             PG8_LDB(B0, 1, 0); PG8_LDB(B1, 1, 1); PG8_SCHED; PG8_LDA(At, 1, 0); PG8_STAGE(PG8_SA(0, 1), rA2, a2 + hstep, voffA);
;             PG8_WAIT_V(8); PG8_WAIT_L(0); PG8_BAR; PG8_MMA(0, 0, At, B0); PG8_MMA(0, 1, At, B1); PG8_BAR; PG8_SCHED;
;             PG8_LDA(At, 1, 1); PG8_STAGE(PG8_SB(1, 0), rB2, b3, voffB); PG8_STAGE(PG8_SB(1, 1), rB2, b3 + hstep, voffB); PG8_STAGE(PG8_SA(1, 0), rA2, a3, voffA);
;             PG8_WAIT_V(8); PG8_WAIT_L(0); PG8_BAR; PG8_MMA(1, 0, At, B0); PG8_MMA(1, 1, At, B1); PG8_BAR; PG8_SCHED;
.LBB0_258:
	ds_read_b128 v[128:131], v252
	ds_read_b128 v[132:135], v252 offset:1024
	ds_read_b128 v[136:139], v252 offset:2048
	ds_read_b128 v[140:143], v252 offset:3072
	ds_read_b128 v[144:147], v225
	ds_read_b128 v[148:151], v225 offset:1024
	ds_read_b128 v[152:155], v225 offset:2048
	ds_read_b128 v[156:159], v225 offset:3072
	s_add_i32 s6, s16, 0x80
	s_cmp_eq_u32 s18, s29
	s_cselect_b32 s46, s2, s6
	s_cselect_b32 s31, s3, s28
	s_or_b32 s30, s46, 0x80
	s_add_i32 s6, s41, s16
	s_mov_b32 m0, s19
	ds_read_b128 v[176:179], v172
	ds_read_b128 v[180:183], v172 offset:1024
	ds_read_b128 v[184:187], v172 offset:2048
	ds_read_b128 v[188:191], v172 offset:3072
	ds_read_b128 v[194:197], v172 offset:4096
	ds_read_b128 v[198:201], v172 offset:5120
	ds_read_b128 v[202:205], v172 offset:6144
	ds_read_b128 v[206:209], v172 offset:7168
	buffer_load_dwordx4 v192, s[36:39], s6 offen lds
	s_mov_b32 m0, s20
	s_nop 0
	buffer_load_dwordx4 v223, s[36:39], s6 offen lds
	s_waitcnt vmcnt(8)
	s_waitcnt lgkmcnt(0)
	s_barrier
	s_setprio 1
	s_waitcnt lgkmcnt(6)
	v_mfma_f32_16x16x128_f8f6f4 v[124:127], v[128:135], v[176:183], v[124:127]
	v_mfma_f32_16x16x128_f8f6f4 v[120:123], v[136:143], v[176:183], v[120:123]
	s_waitcnt lgkmcnt(4)
	v_mfma_f32_16x16x128_f8f6f4 v[108:111], v[128:135], v[184:191], v[108:111]
	v_mfma_f32_16x16x128_f8f6f4 v[104:107], v[136:143], v[184:191], v[104:107]
	s_waitcnt lgkmcnt(2)
	v_mfma_f32_16x16x128_f8f6f4 v[160:163], v[128:135], v[194:201], v[92:95]
	v_mfma_f32_16x16x128_f8f6f4 v[210:213], v[136:143], v[194:201], v[88:91]
	s_waitcnt lgkmcnt(0)
	v_mfma_f32_16x16x128_f8f6f4 v[214:217], v[128:135], v[202:209], v[76:79]
	v_mfma_f32_16x16x128_f8f6f4 v[218:221], v[136:143], v[202:209], v[72:75]
	s_setprio 0
	s_setprio 1
	v_mfma_f32_16x16x128_f8f6f4 v[116:119], v[144:151], v[176:183], v[116:119]
	v_mfma_f32_16x16x128_f8f6f4 v[112:115], v[152:159], v[176:183], v[112:115]
	v_mfma_f32_16x16x128_f8f6f4 v[100:103], v[144:151], v[184:191], v[100:103]
	v_mfma_f32_16x16x128_f8f6f4 v[96:99], v[152:159], v[184:191], v[96:99]
	v_mfma_f32_16x16x128_f8f6f4 v[176:179], v[144:151], v[194:201], v[84:87]
	v_mfma_f32_16x16x128_f8f6f4 v[180:183], v[152:159], v[194:201], v[80:83]
	v_mfma_f32_16x16x128_f8f6f4 v[184:187], v[144:151], v[202:209], v[68:71]
	v_mfma_f32_16x16x128_f8f6f4 v[188:191], v[152:159], v[202:209], v[64:67]
	s_setprio 0
	s_barrier
	s_mov_b32 m0, s43
	s_mov_b32 s6, s38
	s_mov_b32 s7, s39
	s_nop 1
	ds_read_b128 v[64:67], v172 offset:16384
	ds_read_b128 v[68:71], v172 offset:17408
	ds_read_b128 v[72:75], v172 offset:18432
	ds_read_b128 v[76:79], v172 offset:19456
	ds_read_b128 v[80:83], v172 offset:20480
	ds_read_b128 v[84:87], v172 offset:21504
	ds_read_b128 v[88:91], v172 offset:22528
	ds_read_b128 v[92:95], v172 offset:23552
	buffer_load_dwordx4 v222, s[4:7], s31 offen lds
	s_mov_b32 m0, s44
	s_add_i32 s47, s31, s41
	buffer_load_dwordx4 v193, s[4:7], s31 offen lds
	s_mov_b32 m0, s45
	s_nop 0
	buffer_load_dwordx4 v222, s[4:7], s47 offen lds
	s_mov_b32 m0, s52
	s_nop 0
	buffer_load_dwordx4 v193, s[4:7], s47 offen lds
	s_mov_b32 m0, s42
	s_nop 0
	buffer_load_dwordx4 v192, s[36:39], s46 offen lds
	s_mov_b32 m0, s53
	s_nop 0
	buffer_load_dwordx4 v223, s[36:39], s46 offen lds
	s_waitcnt vmcnt(8)
	s_waitcnt lgkmcnt(0)
	s_barrier
	s_setprio 1
	s_waitcnt lgkmcnt(6)
	v_mfma_f32_16x16x128_f8f6f4 v[60:63], v[128:135], v[64:71], v[60:63]
	v_mfma_f32_16x16x128_f8f6f4 v[56:59], v[136:143], v[64:71], v[56:59]
	s_waitcnt lgkmcnt(4)
	v_mfma_f32_16x16x128_f8f6f4 v[194:197], v[128:135], v[72:79], v[44:47]
	v_mfma_f32_16x16x128_f8f6f4 v[198:201], v[136:143], v[72:79], v[40:43]
	s_waitcnt lgkmcnt(2)
	v_mfma_f32_16x16x128_f8f6f4 v[202:205], v[128:135], v[80:87], v[28:31]
	v_mfma_f32_16x16x128_f8f6f4 v[206:209], v[136:143], v[80:87], v[24:27]
	s_waitcnt lgkmcnt(0)
	v_mfma_f32_16x16x128_f8f6f4 v[236:239], v[128:135], v[88:95], v[12:15]
	v_mfma_f32_16x16x128_f8f6f4 v[240:243], v[136:143], v[88:95], v[8:11]
	s_setprio 0
	s_setprio 1
	v_mfma_f32_16x16x128_f8f6f4 v[52:55], v[144:151], v[64:71], v[52:55]
	v_mfma_f32_16x16x128_f8f6f4 v[48:51], v[152:159], v[64:71], v[48:51]
	v_mfma_f32_16x16x128_f8f6f4 v[244:247], v[144:151], v[72:79], v[36:39]
	v_mfma_f32_16x16x128_f8f6f4 v[248:251], v[152:159], v[72:79], v[32:35]
	v_mfma_f32_16x16x128_f8f6f4 v[226:229], v[144:151], v[80:87], v[20:23]
	v_mfma_f32_16x16x128_f8f6f4 v[232:235], v[152:159], v[80:87], v[16:19]
	v_mfma_f32_16x16x128_f8f6f4 v[164:167], v[144:151], v[88:95], v[4:7]
	v_mfma_f32_16x16x128_f8f6f4 v[168:171], v[152:159], v[88:95], v[0:3]
	s_setprio 0
	s_barrier
; #define PG8_STAGE(bufoff, rs_, soff_, voff) do { _Pragma("unroll") for (int _i = 0; _i < 2; ++_i) \
;         __builtin_amdgcn_raw_ptr_buffer_load_lds(rs_, (LAS void*)(lds + (bufoff) + ldsw + _i * 8192), 16, (int)(voff)[_i], (int)(soff_), 0, 0); } while (0)
; #define PG8_LDA(dst, b, h) do { _Pragma("unroll") for (int m = 0; m < 4; ++m) dst[m] = PG8_LD2(lds + PG8_SA(b, h) + aoff + m * 2048); } while (0)
; #define PG8_LDB(dst, b, h) do { _Pragma("unroll") for (int n = 0; n < 2; ++n) dst[n] = PG8_LD2(lds + PG8_SB(b, h) + boff + n * 2048); } while (0)
; #define PG8_WAIT_V(n) asm volatile("s_waitcnt vmcnt(" #n ")" ::: "memory")
; #define PG8_WAIT_L(n) asm volatile("s_waitcnt lgkmcnt(" #n ")" ::: "memory")
; #define PG8_BAR __builtin_amdgcn_s_barrier()
; #define PG8_SCHED __builtin_amdgcn_sched_barrier(0)
; template <class Epi, class Sched, bool ALIGN_EPI = false, bool SP2 = false, bool FP8 = false>
; __device__ __forceinline__ void gemm_phase(LAS unsigned char* lds, const Gemm g, const Sched& S, const Epi& E, int wbase) {
;     ...
;         for (int t = 0; t < nt; t += 2) {
;             const bool last = (t == nt - 2);
;             const unsigned a1 = cA + (unsigned)(t + 1) * kstep;
;             const unsigned a2 = last ? nA : cA + (unsigned)(t + 2) * kstep, b2 = last ? nB : cB + (unsigned)(t + 2) * kstep; const rsrc_t rA2 = (Sched::TWO && last) ? rAn : rAc, rB2 = (Sched::TWO && last) ? rBn : rBc;
;     ...
;             PG8_LDB(B0, 1, 0); PG8_LDB(B1, 1, 1); PG8_SCHED; PG8_LDA(At, 1, 0); PG8_STAGE(PG8_SA(0, 1), rA2, a2 + hstep, voffA);
;             PG8_WAIT_V(8); PG8_WAIT_L(0); PG8_BAR; PG8_MMA(0, 0, At, B0); PG8_MMA(0, 1, At, B1); PG8_BAR; PG8_SCHED;
;             PG8_LDA(At, 1, 1); PG8_STAGE(PG8_SB(1, 0), rB2, b3, voffB); PG8_STAGE(PG8_SB(1, 1), rB2, b3 + hstep, voffB); PG8_STAGE(PG8_SA(1, 0), rA2, a3, voffA);
;             PG8_WAIT_V(8); PG8_WAIT_L(0); PG8_BAR; PG8_MMA(1, 0, At, B0); PG8_MMA(1, 1, At, B1); PG8_BAR; PG8_SCHED;
	s_nop 4
	ds_read_b128 v[0:3], v173
	ds_read_b128 v[4:7], v173 offset:1024
	ds_read_b128 v[16:19], v173 offset:2048
	ds_read_b128 v[20:23], v173 offset:3072
	ds_read_b128 v[128:131], v174
	ds_read_b128 v[132:135], v174 offset:1024
	ds_read_b128 v[136:139], v174 offset:2048
	ds_read_b128 v[140:143], v174 offset:3072
	s_add_i32 s46, s46, s41
	s_mov_b32 m0, s56
	ds_read_b128 v[8:11], v172 offset:32768
	ds_read_b128 v[12:15], v172 offset:33792
	ds_read_b128 v[24:27], v172 offset:34816
	ds_read_b128 v[28:31], v172 offset:35840
	ds_read_b128 v[32:35], v172 offset:36864
	ds_read_b128 v[36:39], v172 offset:37888
	ds_read_b128 v[40:43], v172 offset:38912
	ds_read_b128 v[44:47], v172 offset:39936
	buffer_load_dwordx4 v192, s[36:39], s46 offen lds
	s_mov_b32 m0, s57
	s_nop 0
	buffer_load_dwordx4 v223, s[36:39], s46 offen lds
	s_waitcnt vmcnt(8)
	s_waitcnt lgkmcnt(0)
	s_barrier
	s_setprio 1
	s_waitcnt lgkmcnt(6)
	v_mfma_f32_16x16x128_f8f6f4 v[124:127], v[0:7], v[8:15], v[124:127]
	v_mfma_f32_16x16x128_f8f6f4 v[120:123], v[16:23], v[8:15], v[120:123]
	s_waitcnt lgkmcnt(4)
	v_mfma_f32_16x16x128_f8f6f4 v[108:111], v[0:7], v[24:31], v[108:111]
	v_mfma_f32_16x16x128_f8f6f4 v[104:107], v[16:23], v[24:31], v[104:107]
	s_waitcnt lgkmcnt(2)
	v_mfma_f32_16x16x128_f8f6f4 v[92:95], v[0:7], v[32:39], v[160:163]
	v_mfma_f32_16x16x128_f8f6f4 v[88:91], v[16:23], v[32:39], v[210:213]
	s_waitcnt lgkmcnt(0)
	v_mfma_f32_16x16x128_f8f6f4 v[76:79], v[0:7], v[40:47], v[214:217]
	v_mfma_f32_16x16x128_f8f6f4 v[72:75], v[16:23], v[40:47], v[218:221]
	s_setprio 0
	s_setprio 1
	v_mfma_f32_16x16x128_f8f6f4 v[116:119], v[128:135], v[8:15], v[116:119]
	v_mfma_f32_16x16x128_f8f6f4 v[112:115], v[136:143], v[8:15], v[112:115]
	v_mfma_f32_16x16x128_f8f6f4 v[100:103], v[128:135], v[24:31], v[100:103]
	v_mfma_f32_16x16x128_f8f6f4 v[96:99], v[136:143], v[24:31], v[96:99]
	v_mfma_f32_16x16x128_f8f6f4 v[84:87], v[128:135], v[32:39], v[176:179]
	v_mfma_f32_16x16x128_f8f6f4 v[80:83], v[136:143], v[32:39], v[180:183]
	v_mfma_f32_16x16x128_f8f6f4 v[68:71], v[128:135], v[40:47], v[184:187]
	v_mfma_f32_16x16x128_f8f6f4 v[64:67], v[136:143], v[40:47], v[188:191]
	s_setprio 0
	s_barrier
	s_mov_b32 m0, s58
	s_bitset1_b32 s31, 7
	ds_read_b128 v[32:35], v172 offset:49152
	ds_read_b128 v[36:39], v172 offset:50176
	ds_read_b128 v[144:147], v172 offset:51200
	ds_read_b128 v[148:151], v172 offset:52224
	ds_read_b128 v[152:155], v172 offset:53248
	ds_read_b128 v[156:159], v172 offset:54272
	ds_read_b128 v[176:179], v172 offset:55296
	ds_read_b128 v[180:183], v172 offset:56320
	buffer_load_dwordx4 v222, s[4:7], s31 offen lds
	s_mov_b32 m0, s59
	s_nop 0
	buffer_load_dwordx4 v193, s[4:7], s31 offen lds
	s_add_i32 s31, s31, s41
	s_mov_b32 m0, s65
	s_nop 0
	buffer_load_dwordx4 v222, s[4:7], s31 offen lds
	s_mov_b32 m0, s33
	s_nop 0
	buffer_load_dwordx4 v193, s[4:7], s31 offen lds
	s_mov_b32 m0, s12
	s_nop 0
	buffer_load_dwordx4 v192, s[36:39], s30 offen lds
	s_mov_b32 m0, s13
	s_nop 0
	buffer_load_dwordx4 v223, s[36:39], s30 offen lds
	s_waitcnt vmcnt(8)
	s_waitcnt lgkmcnt(0)
	s_barrier
	s_setprio 1
	s_waitcnt lgkmcnt(6)
	v_mfma_f32_16x16x128_f8f6f4 v[60:63], v[0:7], v[32:39], v[60:63]
	v_mfma_f32_16x16x128_f8f6f4 v[56:59], v[16:23], v[32:39], v[56:59]
	s_waitcnt lgkmcnt(4)
	v_mfma_f32_16x16x128_f8f6f4 v[44:47], v[0:7], v[144:151], v[194:197]
	v_mfma_f32_16x16x128_f8f6f4 v[40:43], v[16:23], v[144:151], v[198:201]
	s_waitcnt lgkmcnt(2)
	v_mfma_f32_16x16x128_f8f6f4 v[28:31], v[0:7], v[152:159], v[202:205]
	v_mfma_f32_16x16x128_f8f6f4 v[24:27], v[16:23], v[152:159], v[206:209]
	s_waitcnt lgkmcnt(0)
	v_mfma_f32_16x16x128_f8f6f4 v[12:15], v[0:7], v[176:183], v[236:239]
	v_mfma_f32_16x16x128_f8f6f4 v[8:11], v[16:23], v[176:183], v[240:243]
	s_setprio 0
	s_setprio 1
	v_mfma_f32_16x16x128_f8f6f4 v[52:55], v[128:135], v[32:39], v[52:55]
	v_mfma_f32_16x16x128_f8f6f4 v[48:51], v[136:143], v[32:39], v[48:51]
	v_mfma_f32_16x16x128_f8f6f4 v[36:39], v[128:135], v[144:151], v[244:247]
	v_mfma_f32_16x16x128_f8f6f4 v[32:35], v[136:143], v[144:151], v[248:251]
	v_mfma_f32_16x16x128_f8f6f4 v[20:23], v[128:135], v[152:159], v[226:229]
	v_mfma_f32_16x16x128_f8f6f4 v[16:19], v[136:143], v[152:159], v[232:235]
	v_mfma_f32_16x16x128_f8f6f4 v[4:7], v[128:135], v[176:183], v[164:167]
	v_mfma_f32_16x16x128_f8f6f4 v[0:3], v[136:143], v[176:183], v[168:171]
	s_setprio 0
	s_barrier
	s_add_i32 s29, s29, 2
	s_addk_i32 s16, 0x100
	s_addk_i32 s28, 0x100
	s_cmp_ge_i32 s29, s77
	s_cbranch_scc0 .LBB0_258
	v_mov_b32_e32 v233, v175
	v_mov_b32_e32 v234, v230
	v_mov_b32_e32 v164, v231
	v_mov_b32_e32 v231, 1
	v_mov_b32_e32 v230, 0x358637bd
	s_and_b64 vcc, exec, s[78:79]
	s_cbranch_vccnz .LBB0_261
	s_branch .LBB0_262

; #define PG8_STAGE(bufoff, rs_, soff_, voff) do { _Pragma("unroll") for (int _i = 0; _i < 2; ++_i) \
;         __builtin_amdgcn_raw_ptr_buffer_load_lds(rs_, (LAS void*)(lds + (bufoff) + ldsw + _i * 8192), 16, (int)(voff)[_i], (int)(soff_), 0, 0); } while (0)
; #define PG8_LDA(dst, b, h) do { _Pragma("unroll") for (int m = 0; m < 4; ++m) dst[m] = PG8_LD2(lds + PG8_SA(b, h) + aoff + m * 2048); } while (0)
; #define PG8_LDB(dst, b, h) do { _Pragma("unroll") for (int n = 0; n < 2; ++n) dst[n] = PG8_LD2(lds + PG8_SB(b, h) + boff + n * 2048); } while (0)
; #define PG8_WAIT_V(n) asm volatile("s_waitcnt vmcnt(" #n ")" ::: "memory")
; #define PG8_WAIT_L(n) asm volatile("s_waitcnt lgkmcnt(" #n ")" ::: "memory")
; #define PG8_BAR __builtin_amdgcn_s_barrier()
; #define PG8_SCHED __builtin_amdgcn_sched_barrier(0)
; template <class Epi, class Sched, bool ALIGN_EPI = false, bool SP2 = false, bool FP8 = false>
; __device__ __forceinline__ void gemm_phase(LAS unsigned char* lds, const Gemm g, const Sched& S, const Epi& E, int wbase) {
;     ...
;             PG8_LDB(B0, 0, 0); PG8_LDB(B1, 0, 1); PG8_SCHED; PG8_LDA(At, 0, 0); PG8_STAGE(PG8_SA(1, 1), rAc, a1 + hstep, voffA);
;             PG8_WAIT_V(8); PG8_WAIT_L(0); PG8_BAR; PG8_MMA(0, 0, At, B0); PG8_MMA(0, 1, At, B1); PG8_BAR; PG8_SCHED;
;             PG8_LDA(At, 0, 1); PG8_STAGE(PG8_SB(0, 0), rB2, b2, voffB); PG8_STAGE(PG8_SB(0, 1), rB2, b2 + hstep, voffB); PG8_STAGE(PG8_SA(0, 0), rA2, a2, voffA);
;             PG8_WAIT_V(8); PG8_WAIT_L(0); PG8_BAR; PG8_MMA(1, 0, At, B0); PG8_MMA(1, 1, At, B1); PG8_BAR; PG8_SCHED;
;             PG8_LDB(B0, 1, 0); PG8_LDB(B1, 1, 1); PG8_SCHED; PG8_LDA(At, 1, 0); PG8_STAGE(PG8_SA(0, 1), rA2, a2 + hstep, voffA);
;             PG8_WAIT_V(8); PG8_WAIT_L(0); PG8_BAR; PG8_MMA(0, 0, At, B0); PG8_MMA(0, 1, At, B1); PG8_BAR; PG8_SCHED;
;             PG8_LDA(At, 1, 1); PG8_STAGE(PG8_SB(1, 0), rB2, b3, voffB); PG8_STAGE(PG8_SB(1, 1), rB2, b3 + hstep, voffB); PG8_STAGE(PG8_SA(1, 0), rA2, a3, voffA);
;             PG8_WAIT_V(8); PG8_WAIT_L(0); PG8_BAR; PG8_MMA(1, 0, At, B0); PG8_MMA(1, 1, At, B1); PG8_BAR; PG8_SCHED;
.LBB0_813:
	s_add_i32 s20, vcc_hi, 0x80
	v_add_u32_e32 v140, 0x10000, v240
	v_add_u32_e32 v156, 0x14000, v240
	s_cmp_eq_u32 s41, s78
	ds_read_b128 v[128:131], v140
	ds_read_b128 v[132:135], v140 offset:1024
	ds_read_b128 v[136:139], v140 offset:2048
	ds_read_b128 v[140:143], v140 offset:3072
	ds_read_b128 v[144:147], v156
	ds_read_b128 v[148:151], v156 offset:1024
	ds_read_b128 v[152:155], v156 offset:2048
	ds_read_b128 v[156:159], v156 offset:3072
	s_cselect_b64 s[16:17], -1, 0
	s_and_b64 s[18:19], s[16:17], exec
	s_cselect_b32 s68, s67, s20
	s_cselect_b32 s54, vcc_lo, s3
	s_and_b64 s[20:21], s[44:45], s[16:17]
	s_and_b64 s[16:17], s[20:21], exec
	s_cselect_b32 s18, s52, s14
	s_cselect_b32 s19, s53, s15
	s_cselect_b32 s17, s35, s13
	s_cselect_b32 s16, s34, s12
	s_or_b32 s55, s68, 0x80
	s_and_b64 s[20:21], s[20:21], exec
	s_cselect_b32 s23, s53, s31
	s_cselect_b32 s22, s52, s30
	s_cselect_b32 s21, s11, s59
	s_cselect_b32 s20, s10, s58
	s_add_i32 s69, s46, vcc_hi
	s_mov_b32 m0, s61
	ds_read_b128 v[160:163], v241
	ds_read_b128 v[164:167], v241 offset:1024
	ds_read_b128 v[168:171], v241 offset:2048
	ds_read_b128 v[172:175], v241 offset:3072
	ds_read_b128 v[176:179], v241 offset:4096
	ds_read_b128 v[180:183], v241 offset:5120
	ds_read_b128 v[184:187], v241 offset:6144
	ds_read_b128 v[188:191], v241 offset:7168
	buffer_load_dwordx4 v192, s[12:15], s69 offen lds
	s_mov_b32 m0, s62
	s_nop 0
	buffer_load_dwordx4 v236, s[12:15], s69 offen lds
	s_waitcnt vmcnt(8)
	s_waitcnt lgkmcnt(0)
	s_barrier
	s_setprio 1
	s_waitcnt lgkmcnt(6)
	v_mfma_f32_16x16x128_f8f6f4 v[124:127], v[128:135], v[160:167], v[124:127]
	v_mfma_f32_16x16x128_f8f6f4 v[120:123], v[136:143], v[160:167], v[120:123]
	s_waitcnt lgkmcnt(4)
	v_mfma_f32_16x16x128_f8f6f4 v[116:119], v[128:135], v[168:175], v[116:119]
	v_mfma_f32_16x16x128_f8f6f4 v[112:115], v[136:143], v[168:175], v[112:115]
	s_waitcnt lgkmcnt(2)
	v_mfma_f32_16x16x128_f8f6f4 v[108:111], v[128:135], v[176:183], v[108:111]
	v_mfma_f32_16x16x128_f8f6f4 v[104:107], v[136:143], v[176:183], v[104:107]
	s_waitcnt lgkmcnt(0)
	v_mfma_f32_16x16x128_f8f6f4 v[100:103], v[128:135], v[184:191], v[100:103]
	v_mfma_f32_16x16x128_f8f6f4 v[96:99], v[136:143], v[184:191], v[96:99]
	s_setprio 0
	s_setprio 1
	v_mfma_f32_16x16x128_f8f6f4 v[194:197], v[144:151], v[160:167], v[92:95]
	v_mfma_f32_16x16x128_f8f6f4 v[160:163], v[152:159], v[160:167], v[88:91]
	v_mfma_f32_16x16x128_f8f6f4 v[164:167], v[144:151], v[168:175], v[84:87]
	v_mfma_f32_16x16x128_f8f6f4 v[168:171], v[152:159], v[168:175], v[80:83]
	v_mfma_f32_16x16x128_f8f6f4 v[172:175], v[144:151], v[176:183], v[76:79]
	v_mfma_f32_16x16x128_f8f6f4 v[176:179], v[152:159], v[176:183], v[72:75]
	v_mfma_f32_16x16x128_f8f6f4 v[180:183], v[144:151], v[184:191], v[68:71]
	v_mfma_f32_16x16x128_f8f6f4 v[184:187], v[152:159], v[184:191], v[64:67]
	s_setprio 0
	s_barrier
	s_mov_b32 m0, s48
	s_nop 3
	ds_read_b128 v[64:67], v241 offset:16384
	ds_read_b128 v[68:71], v241 offset:17408
	ds_read_b128 v[72:75], v241 offset:18432
	ds_read_b128 v[76:79], v241 offset:19456
	ds_read_b128 v[80:83], v241 offset:20480
	ds_read_b128 v[84:87], v241 offset:21504
	ds_read_b128 v[88:91], v241 offset:22528
	ds_read_b128 v[92:95], v241 offset:23552
	buffer_load_dwordx4 v235, s[20:23], s54 offen lds
	s_mov_b32 m0, s56
	s_add_i32 s69, s54, s46
	buffer_load_dwordx4 v237, s[20:23], s54 offen lds
	s_mov_b32 m0, s57
	s_nop 0
	buffer_load_dwordx4 v235, s[20:23], s69 offen lds
	s_mov_b32 m0, s65
	s_nop 0
	buffer_load_dwordx4 v237, s[20:23], s69 offen lds
	s_mov_b32 m0, s47
	s_nop 0
	buffer_load_dwordx4 v192, s[16:19], s68 offen lds
	s_mov_b32 m0, s76
	s_nop 0
	buffer_load_dwordx4 v236, s[16:19], s68 offen lds
	s_waitcnt vmcnt(8)
	s_waitcnt lgkmcnt(0)
	s_barrier
	s_setprio 1
	s_waitcnt lgkmcnt(6)
	v_mfma_f32_16x16x128_f8f6f4 v[60:63], v[128:135], v[64:71], v[60:63]
	v_mfma_f32_16x16x128_f8f6f4 v[56:59], v[136:143], v[64:71], v[56:59]
	s_waitcnt lgkmcnt(4)
	v_mfma_f32_16x16x128_f8f6f4 v[52:55], v[128:135], v[72:79], v[52:55]
	v_mfma_f32_16x16x128_f8f6f4 v[48:51], v[136:143], v[72:79], v[48:51]
	s_waitcnt lgkmcnt(2)
	v_mfma_f32_16x16x128_f8f6f4 v[188:191], v[128:135], v[80:87], v[44:47]
	v_mfma_f32_16x16x128_f8f6f4 v[198:201], v[136:143], v[80:87], v[40:43]
	s_waitcnt lgkmcnt(0)
	v_mfma_f32_16x16x128_f8f6f4 v[202:205], v[128:135], v[88:95], v[36:39]
	v_mfma_f32_16x16x128_f8f6f4 v[206:209], v[136:143], v[88:95], v[32:35]
	s_setprio 0
	s_setprio 1
	v_mfma_f32_16x16x128_f8f6f4 v[210:213], v[144:151], v[64:71], v[28:31]
	v_mfma_f32_16x16x128_f8f6f4 v[214:217], v[152:159], v[64:71], v[24:27]
	v_mfma_f32_16x16x128_f8f6f4 v[218:221], v[144:151], v[72:79], v[20:23]
	v_mfma_f32_16x16x128_f8f6f4 v[226:229], v[152:159], v[72:79], v[16:19]
	v_mfma_f32_16x16x128_f8f6f4 v[242:245], v[144:151], v[80:87], v[12:15]
	v_mfma_f32_16x16x128_f8f6f4 v[246:249], v[152:159], v[80:87], v[8:11]
	v_mfma_f32_16x16x128_f8f6f4 v[250:253], v[144:151], v[88:95], v[4:7]
	v_mfma_f32_16x16x128_f8f6f4 v[230:233], v[152:159], v[88:95], v[0:3]
	s_setprio 0
	s_barrier
; #define PG8_STAGE(bufoff, rs_, soff_, voff) do { _Pragma("unroll") for (int _i = 0; _i < 2; ++_i) \
;         __builtin_amdgcn_raw_ptr_buffer_load_lds(rs_, (LAS void*)(lds + (bufoff) + ldsw + _i * 8192), 16, (int)(voff)[_i], (int)(soff_), 0, 0); } while (0)
; #define PG8_LDA(dst, b, h) do { _Pragma("unroll") for (int m = 0; m < 4; ++m) dst[m] = PG8_LD2(lds + PG8_SA(b, h) + aoff + m * 2048); } while (0)
; #define PG8_LDB(dst, b, h) do { _Pragma("unroll") for (int n = 0; n < 2; ++n) dst[n] = PG8_LD2(lds + PG8_SB(b, h) + boff + n * 2048); } while (0)
; #define PG8_WAIT_V(n) asm volatile("s_waitcnt vmcnt(" #n ")" ::: "memory")
; #define PG8_WAIT_L(n) asm volatile("s_waitcnt lgkmcnt(" #n ")" ::: "memory")
; #define PG8_BAR __builtin_amdgcn_s_barrier()
; #define PG8_SCHED __builtin_amdgcn_sched_barrier(0)
; template <class Epi, class Sched, bool ALIGN_EPI = false, bool SP2 = false, bool FP8 = false>
; __device__ __forceinline__ void gemm_phase(LAS unsigned char* lds, const Gemm g, const Sched& S, const Epi& E, int wbase) {
;     ...
;         for (int t = 0; t < nt; t += 2) {
;             const bool last = (t == nt - 2);
;             const unsigned a1 = cA + (unsigned)(t + 1) * kstep;
;             const unsigned a2 = last ? nA : cA + (unsigned)(t + 2) * kstep, b2 = last ? nB : cB + (unsigned)(t + 2) * kstep; const rsrc_t rA2 = (Sched::TWO && last) ? rAn : rAc, rB2 = (Sched::TWO && last) ? rBn : rBc;
;     ...
;             PG8_LDB(B0, 1, 0); PG8_LDB(B1, 1, 1); PG8_SCHED; PG8_LDA(At, 1, 0); PG8_STAGE(PG8_SA(0, 1), rA2, a2 + hstep, voffA);
;             PG8_WAIT_V(8); PG8_WAIT_L(0); PG8_BAR; PG8_MMA(0, 0, At, B0); PG8_MMA(0, 1, At, B1); PG8_BAR; PG8_SCHED;
;             PG8_LDA(At, 1, 1); PG8_STAGE(PG8_SB(1, 0), rB2, b3, voffB); PG8_STAGE(PG8_SB(1, 1), rB2, b3 + hstep, voffB); PG8_STAGE(PG8_SA(1, 0), rA2, a3, voffA);
;             PG8_WAIT_V(8); PG8_WAIT_L(0); PG8_BAR; PG8_MMA(1, 0, At, B0); PG8_MMA(1, 1, At, B1); PG8_BAR; PG8_SCHED;
	s_nop 1
	v_add_u32_e32 v12, 0x18000, v240
	v_add_u32_e32 v16, 0x1c000, v240
	s_nop 0
	ds_read_b128 v[0:3], v12
	ds_read_b128 v[4:7], v12 offset:1024
	ds_read_b128 v[8:11], v12 offset:2048
	ds_read_b128 v[12:15], v12 offset:3072
	ds_read_b128 v[128:131], v16
	ds_read_b128 v[132:135], v16 offset:1024
	ds_read_b128 v[136:139], v16 offset:2048
	ds_read_b128 v[140:143], v16 offset:3072
	s_add_i32 s68, s68, s46
	s_mov_b32 m0, s77
	ds_read_b128 v[16:19], v241 offset:32768
	ds_read_b128 v[20:23], v241 offset:33792
	ds_read_b128 v[24:27], v241 offset:34816
	ds_read_b128 v[28:31], v241 offset:35840
	ds_read_b128 v[32:35], v241 offset:36864
	ds_read_b128 v[36:39], v241 offset:37888
	ds_read_b128 v[40:43], v241 offset:38912
	ds_read_b128 v[44:47], v241 offset:39936
	buffer_load_dwordx4 v192, s[16:19], s68 offen lds
	s_mov_b32 m0, s79
	s_nop 0
	buffer_load_dwordx4 v236, s[16:19], s68 offen lds
	s_waitcnt vmcnt(8)
	s_waitcnt lgkmcnt(0)
	s_barrier
	s_setprio 1
	s_waitcnt lgkmcnt(6)
	v_mfma_f32_16x16x128_f8f6f4 v[124:127], v[0:7], v[16:23], v[124:127]
	v_mfma_f32_16x16x128_f8f6f4 v[120:123], v[8:15], v[16:23], v[120:123]
	s_waitcnt lgkmcnt(4)
	v_mfma_f32_16x16x128_f8f6f4 v[116:119], v[0:7], v[24:31], v[116:119]
	v_mfma_f32_16x16x128_f8f6f4 v[112:115], v[8:15], v[24:31], v[112:115]
	s_waitcnt lgkmcnt(2)
	v_mfma_f32_16x16x128_f8f6f4 v[108:111], v[0:7], v[32:39], v[108:111]
	v_mfma_f32_16x16x128_f8f6f4 v[104:107], v[8:15], v[32:39], v[104:107]
	s_waitcnt lgkmcnt(0)
	v_mfma_f32_16x16x128_f8f6f4 v[100:103], v[0:7], v[40:47], v[100:103]
	v_mfma_f32_16x16x128_f8f6f4 v[96:99], v[8:15], v[40:47], v[96:99]
	s_setprio 0
	s_setprio 1
	v_mfma_f32_16x16x128_f8f6f4 v[92:95], v[128:135], v[16:23], v[194:197]
	v_mfma_f32_16x16x128_f8f6f4 v[88:91], v[136:143], v[16:23], v[160:163]
	v_mfma_f32_16x16x128_f8f6f4 v[84:87], v[128:135], v[24:31], v[164:167]
	v_mfma_f32_16x16x128_f8f6f4 v[80:83], v[136:143], v[24:31], v[168:171]
	v_mfma_f32_16x16x128_f8f6f4 v[76:79], v[128:135], v[32:39], v[172:175]
	v_mfma_f32_16x16x128_f8f6f4 v[72:75], v[136:143], v[32:39], v[176:179]
	v_mfma_f32_16x16x128_f8f6f4 v[68:71], v[128:135], v[40:47], v[180:183]
	v_mfma_f32_16x16x128_f8f6f4 v[64:67], v[136:143], v[40:47], v[184:187]
	s_setprio 0
	s_barrier
	s_mov_b32 m0, s84
	s_bitset1_b32 s54, 7
	ds_read_b128 v[16:19], v241 offset:49152
	ds_read_b128 v[20:23], v241 offset:50176
	ds_read_b128 v[144:147], v241 offset:51200
	ds_read_b128 v[148:151], v241 offset:52224
	ds_read_b128 v[152:155], v241 offset:53248
	ds_read_b128 v[156:159], v241 offset:54272
	ds_read_b128 v[160:163], v241 offset:55296
	ds_read_b128 v[164:167], v241 offset:56320
	buffer_load_dwordx4 v235, s[20:23], s54 offen lds
	s_mov_b32 m0, s85
	s_nop 0
	buffer_load_dwordx4 v237, s[20:23], s54 offen lds
	s_add_i32 s54, s54, s46
	s_mov_b32 m0, s96
	s_nop 0
	buffer_load_dwordx4 v235, s[20:23], s54 offen lds
	s_mov_b32 m0, s97
	s_nop 0
	buffer_load_dwordx4 v237, s[20:23], s54 offen lds
	s_mov_b32 m0, s94
	s_nop 0
	buffer_load_dwordx4 v192, s[16:19], s55 offen lds
	s_mov_b32 m0, s95
	s_nop 0
	buffer_load_dwordx4 v236, s[16:19], s55 offen lds
	s_waitcnt vmcnt(8)
	s_waitcnt lgkmcnt(0)
	s_barrier
	s_setprio 1
	s_waitcnt lgkmcnt(6)
	v_mfma_f32_16x16x128_f8f6f4 v[60:63], v[0:7], v[16:23], v[60:63]
	v_mfma_f32_16x16x128_f8f6f4 v[56:59], v[8:15], v[16:23], v[56:59]
	s_waitcnt lgkmcnt(4)
	v_mfma_f32_16x16x128_f8f6f4 v[52:55], v[0:7], v[144:151], v[52:55]
	v_mfma_f32_16x16x128_f8f6f4 v[48:51], v[8:15], v[144:151], v[48:51]
	s_waitcnt lgkmcnt(2)
	v_mfma_f32_16x16x128_f8f6f4 v[44:47], v[0:7], v[152:159], v[188:191]
	v_mfma_f32_16x16x128_f8f6f4 v[40:43], v[8:15], v[152:159], v[198:201]
	s_waitcnt lgkmcnt(0)
	v_mfma_f32_16x16x128_f8f6f4 v[36:39], v[0:7], v[160:167], v[202:205]
	v_mfma_f32_16x16x128_f8f6f4 v[32:35], v[8:15], v[160:167], v[206:209]
	s_setprio 0
	s_setprio 1
	v_mfma_f32_16x16x128_f8f6f4 v[28:31], v[128:135], v[16:23], v[210:213]
	v_mfma_f32_16x16x128_f8f6f4 v[24:27], v[136:143], v[16:23], v[214:217]
	v_mfma_f32_16x16x128_f8f6f4 v[20:23], v[128:135], v[144:151], v[218:221]
	v_mfma_f32_16x16x128_f8f6f4 v[16:19], v[136:143], v[144:151], v[226:229]
	v_mfma_f32_16x16x128_f8f6f4 v[12:15], v[128:135], v[152:159], v[242:245]
	v_mfma_f32_16x16x128_f8f6f4 v[8:11], v[136:143], v[152:159], v[246:249]
	v_mfma_f32_16x16x128_f8f6f4 v[4:7], v[128:135], v[160:167], v[250:253]
	v_mfma_f32_16x16x128_f8f6f4 v[0:3], v[136:143], v[160:167], v[230:233]
	s_setprio 0
	s_barrier
	s_add_i32 s78, s78, 2
	s_addk_i32 vcc_hi, 0x100
	s_addk_i32 s3, 0x100
	s_cmp_ge_i32 s78, s60
	s_cbranch_scc0 .LBB0_813
	v_readlane_b32 s68, v255, 22
	v_readlane_b32 s54, v255, 25
	v_readlane_b32 s69, v255, 23
	v_readlane_b32 s55, v255, 26
	v_mov_b32_e32 v230, v193
	v_mov_b32_e32 v231, v222

; #define PG8_STAGE(bufoff, rs_, soff_, voff) do { _Pragma("unroll") for (int _i = 0; _i < 2; ++_i) \
;         __builtin_amdgcn_raw_ptr_buffer_load_lds(rs_, (LAS void*)(lds + (bufoff) + ldsw + _i * 8192), 16, (int)(voff)[_i], (int)(soff_), 0, 0); } while (0)
; #define PG8_LDA(dst, b, h) do { _Pragma("unroll") for (int m = 0; m < 4; ++m) dst[m] = PG8_LD2(lds + PG8_SA(b, h) + aoff + m * 2048); } while (0)
; #define PG8_LDB(dst, b, h) do { _Pragma("unroll") for (int n = 0; n < 2; ++n) dst[n] = PG8_LD2(lds + PG8_SB(b, h) + boff + n * 2048); } while (0)
; #define PG8_WAIT_V(n) asm volatile("s_waitcnt vmcnt(" #n ")" ::: "memory")
; #define PG8_WAIT_L(n) asm volatile("s_waitcnt lgkmcnt(" #n ")" ::: "memory")
; #define PG8_BAR __builtin_amdgcn_s_barrier()
; #define PG8_SCHED __builtin_amdgcn_sched_barrier(0)
; template <class Epi, class Sched, bool ALIGN_EPI = false, bool SP2 = false, bool FP8 = false>
; __device__ __forceinline__ void gemm_phase(LAS unsigned char* lds, const Gemm g, const Sched& S, const Epi& E, int wbase) {
;     ...
;             PG8_LDB(B0, 0, 0); PG8_LDB(B1, 0, 1); PG8_SCHED; PG8_LDA(At, 0, 0); PG8_STAGE(PG8_SA(1, 1), rAc, a1 + hstep, voffA);
;             PG8_WAIT_V(8); PG8_WAIT_L(0); PG8_BAR; PG8_MMA(0, 0, At, B0); PG8_MMA(0, 1, At, B1); PG8_BAR; PG8_SCHED;
;             PG8_LDA(At, 0, 1); PG8_STAGE(PG8_SB(0, 0), rB2, b2, voffB); PG8_STAGE(PG8_SB(0, 1), rB2, b2 + hstep, voffB); PG8_STAGE(PG8_SA(0, 0), rA2, a2, voffA);
;             PG8_WAIT_V(8); PG8_WAIT_L(0); PG8_BAR; PG8_MMA(1, 0, At, B0); PG8_MMA(1, 1, At, B1); PG8_BAR; PG8_SCHED;
;             PG8_LDB(B0, 1, 0); PG8_LDB(B1, 1, 1); PG8_SCHED; PG8_LDA(At, 1, 0); PG8_STAGE(PG8_SA(0, 1), rA2, a2 + hstep, voffA);
;             PG8_WAIT_V(8); PG8_WAIT_L(0); PG8_BAR; PG8_MMA(0, 0, At, B0); PG8_MMA(0, 1, At, B1); PG8_BAR; PG8_SCHED;
;             PG8_LDA(At, 1, 1); PG8_STAGE(PG8_SB(1, 0), rB2, b3, voffB); PG8_STAGE(PG8_SB(1, 1), rB2, b3 + hstep, voffB); PG8_STAGE(PG8_SA(1, 0), rA2, a3, voffA);
;             PG8_WAIT_V(8); PG8_WAIT_L(0); PG8_BAR; PG8_MMA(1, 0, At, B0); PG8_MMA(1, 1, At, B1); PG8_BAR; PG8_SCHED;
.LBB0_926:
	v_add_u32_e32 v120, 0x10000, v160
	ds_read_b128 v[132:135], v120
	ds_read_b128 v[136:139], v120 offset:1024
	ds_read_b128 v[140:143], v120 offset:2048
	ds_read_b128 v[144:147], v120 offset:3072
	v_add_u32_e32 v120, 0x14000, v160
	ds_read_b128 v[162:165], v120
	ds_read_b128 v[166:169], v120 offset:1024
	ds_read_b128 v[170:173], v120 offset:2048
	ds_read_b128 v[174:177], v120 offset:3072
	s_add_i32 s14, s4, 0x80
	s_cmp_eq_u32 s60, s11
	s_cselect_b32 s66, s2, s14
	s_cselect_b32 s55, s3, s5
	s_or_b32 s54, s66, 0x80
	s_add_i32 s14, s30, s4
	s_mov_b32 m0, s61
	ds_read_b128 v[178:181], v161
	ds_read_b128 v[182:185], v161 offset:1024
	ds_read_b128 v[194:197], v161 offset:2048
	ds_read_b128 v[198:201], v161 offset:3072
	ds_read_b128 v[202:205], v161 offset:4096
	ds_read_b128 v[206:209], v161 offset:5120
	ds_read_b128 v[210:213], v161 offset:6144
	ds_read_b128 v[214:217], v161 offset:7168
	buffer_load_dwordx4 v222, s[36:39], s14 offen lds
	s_mov_b32 m0, s62
	s_nop 0
	buffer_load_dwordx4 v156, s[36:39], s14 offen lds
	s_waitcnt vmcnt(8)
	s_waitcnt lgkmcnt(0)
	s_barrier
	s_setprio 1
	s_waitcnt lgkmcnt(6)
	v_mfma_f32_16x16x128_f8f6f4 v[124:127], v[140:147], v[178:185], v[124:127]
	s_waitcnt lgkmcnt(4)
	v_mfma_f32_16x16x128_f8f6f4 v[108:111], v[132:139], v[194:201], v[108:111]
	v_mfma_f32_16x16x128_f8f6f4 v[104:107], v[140:147], v[194:201], v[104:107]
	v_mfma_f32_16x16x128_f8f6f4 v[120:123], v[132:139], v[178:185], v[128:131]
	s_waitcnt lgkmcnt(2)
	v_mfma_f32_16x16x128_f8f6f4 v[148:151], v[132:139], v[202:209], v[92:95]
	v_mfma_f32_16x16x128_f8f6f4 v[186:189], v[140:147], v[202:209], v[88:91]
	s_waitcnt lgkmcnt(0)
	v_mfma_f32_16x16x128_f8f6f4 v[218:221], v[132:139], v[210:217], v[76:79]
	v_mfma_f32_16x16x128_f8f6f4 v[226:229], v[140:147], v[210:217], v[72:75]
	s_setprio 0
	s_setprio 1
	v_mfma_f32_16x16x128_f8f6f4 v[116:119], v[162:169], v[178:185], v[116:119]
	v_mfma_f32_16x16x128_f8f6f4 v[112:115], v[170:177], v[178:185], v[112:115]
	v_mfma_f32_16x16x128_f8f6f4 v[100:103], v[162:169], v[194:201], v[100:103]
	v_mfma_f32_16x16x128_f8f6f4 v[96:99], v[170:177], v[194:201], v[96:99]
	v_mfma_f32_16x16x128_f8f6f4 v[178:181], v[162:169], v[202:209], v[84:87]
	v_mfma_f32_16x16x128_f8f6f4 v[182:185], v[170:177], v[202:209], v[80:83]
	v_mfma_f32_16x16x128_f8f6f4 v[194:197], v[162:169], v[210:217], v[68:71]
	v_mfma_f32_16x16x128_f8f6f4 v[198:201], v[170:177], v[210:217], v[64:67]
	s_setprio 0
	s_barrier
	s_mov_b32 m0, s33
	s_mov_b32 s14, s38
	s_mov_b32 s15, s39
	s_nop 1
	ds_read_b128 v[64:67], v161 offset:16384
	ds_read_b128 v[68:71], v161 offset:17408
	ds_read_b128 v[72:75], v161 offset:18432
	ds_read_b128 v[76:79], v161 offset:19456
	ds_read_b128 v[80:83], v161 offset:20480
	ds_read_b128 v[84:87], v161 offset:21504
	ds_read_b128 v[88:91], v161 offset:22528
	ds_read_b128 v[92:95], v161 offset:23552
	buffer_load_dwordx4 v223, s[12:15], s55 offen lds
	s_mov_b32 m0, s34
	s_add_i32 s67, s55, s30
	buffer_load_dwordx4 v157, s[12:15], s55 offen lds
	s_mov_b32 m0, s35
	s_nop 0
	buffer_load_dwordx4 v223, s[12:15], s67 offen lds
	s_mov_b32 m0, s41
	s_nop 0
	buffer_load_dwordx4 v157, s[12:15], s67 offen lds
	s_mov_b32 m0, s31
	s_nop 0
	buffer_load_dwordx4 v222, s[36:39], s66 offen lds
	s_mov_b32 m0, s42
	s_nop 0
	buffer_load_dwordx4 v156, s[36:39], s66 offen lds
	s_waitcnt vmcnt(8)
	s_waitcnt lgkmcnt(0)
	s_barrier
	s_setprio 1
	s_waitcnt lgkmcnt(6)
	v_mfma_f32_16x16x128_f8f6f4 v[60:63], v[132:139], v[64:71], v[60:63]
	v_mfma_f32_16x16x128_f8f6f4 v[56:59], v[140:147], v[64:71], v[56:59]
	s_waitcnt lgkmcnt(4)
	v_mfma_f32_16x16x128_f8f6f4 v[202:205], v[132:139], v[72:79], v[44:47]
	v_mfma_f32_16x16x128_f8f6f4 v[206:209], v[140:147], v[72:79], v[40:43]
	s_waitcnt lgkmcnt(2)
	v_mfma_f32_16x16x128_f8f6f4 v[210:213], v[132:139], v[80:87], v[28:31]
	v_mfma_f32_16x16x128_f8f6f4 v[214:217], v[140:147], v[80:87], v[24:27]
	s_waitcnt lgkmcnt(0)
	v_mfma_f32_16x16x128_f8f6f4 v[230:233], v[132:139], v[88:95], v[12:15]
	v_mfma_f32_16x16x128_f8f6f4 v[234:237], v[140:147], v[88:95], v[8:11]
	s_setprio 0
	s_setprio 1
	v_mfma_f32_16x16x128_f8f6f4 v[52:55], v[162:169], v[64:71], v[52:55]
	v_mfma_f32_16x16x128_f8f6f4 v[48:51], v[170:177], v[64:71], v[48:51]
	v_mfma_f32_16x16x128_f8f6f4 v[238:241], v[162:169], v[72:79], v[36:39]
	v_mfma_f32_16x16x128_f8f6f4 v[242:245], v[170:177], v[72:79], v[32:35]
	v_mfma_f32_16x16x128_f8f6f4 v[246:249], v[162:169], v[80:87], v[20:23]
	v_mfma_f32_16x16x128_f8f6f4 v[250:253], v[170:177], v[80:87], v[16:19]
	v_mfma_f32_16x16x128_f8f6f4 v[190:193], v[162:169], v[88:95], v[4:7]
	v_mfma_f32_16x16x128_f8f6f4 v[152:155], v[170:177], v[88:95], v[0:3]
	s_setprio 0
	s_barrier
; #define PG8_STAGE(bufoff, rs_, soff_, voff) do { _Pragma("unroll") for (int _i = 0; _i < 2; ++_i) \
;         __builtin_amdgcn_raw_ptr_buffer_load_lds(rs_, (LAS void*)(lds + (bufoff) + ldsw + _i * 8192), 16, (int)(voff)[_i], (int)(soff_), 0, 0); } while (0)
; #define PG8_LDA(dst, b, h) do { _Pragma("unroll") for (int m = 0; m < 4; ++m) dst[m] = PG8_LD2(lds + PG8_SA(b, h) + aoff + m * 2048); } while (0)
; #define PG8_LDB(dst, b, h) do { _Pragma("unroll") for (int n = 0; n < 2; ++n) dst[n] = PG8_LD2(lds + PG8_SB(b, h) + boff + n * 2048); } while (0)
; #define PG8_WAIT_V(n) asm volatile("s_waitcnt vmcnt(" #n ")" ::: "memory")
; #define PG8_WAIT_L(n) asm volatile("s_waitcnt lgkmcnt(" #n ")" ::: "memory")
; #define PG8_BAR __builtin_amdgcn_s_barrier()
; #define PG8_SCHED __builtin_amdgcn_sched_barrier(0)
; template <class Epi, class Sched, bool ALIGN_EPI = false, bool SP2 = false, bool FP8 = false>
; __device__ __forceinline__ void gemm_phase(LAS unsigned char* lds, const Gemm g, const Sched& S, const Epi& E, int wbase) {
;     ...
;             PG8_LDB(B0, 1, 0); PG8_LDB(B1, 1, 1); PG8_SCHED; PG8_LDA(At, 1, 0); PG8_STAGE(PG8_SA(0, 1), rA2, a2 + hstep, voffA);
;             PG8_WAIT_V(8); PG8_WAIT_L(0); PG8_BAR; PG8_MMA(0, 0, At, B0); PG8_MMA(0, 1, At, B1); PG8_BAR; PG8_SCHED;
;             PG8_LDA(At, 1, 1); PG8_STAGE(PG8_SB(1, 0), rB2, b3, voffB); PG8_STAGE(PG8_SB(1, 1), rB2, b3 + hstep, voffB); PG8_STAGE(PG8_SA(1, 0), rA2, a3, voffA);
;             PG8_WAIT_V(8); PG8_WAIT_L(0); PG8_BAR; PG8_MMA(1, 0, At, B0); PG8_MMA(1, 1, At, B1); PG8_BAR; PG8_SCHED;
	v_add_u32_e32 v8, 0x18000, v160
	s_nop 3
	ds_read_b128 v[0:3], v8
	ds_read_b128 v[4:7], v8 offset:1024
	ds_read_b128 v[16:19], v8 offset:2048
	ds_read_b128 v[20:23], v8 offset:3072
	v_add_u32_e32 v8, 0x1c000, v160
	ds_read_b128 v[132:135], v8
	ds_read_b128 v[136:139], v8 offset:1024
	ds_read_b128 v[140:143], v8 offset:2048
	ds_read_b128 v[144:147], v8 offset:3072
	s_add_i32 s66, s66, s30
	s_mov_b32 m0, s43
	ds_read_b128 v[8:11], v161 offset:32768
	ds_read_b128 v[12:15], v161 offset:33792
	ds_read_b128 v[24:27], v161 offset:34816
	ds_read_b128 v[28:31], v161 offset:35840
	ds_read_b128 v[32:35], v161 offset:36864
	ds_read_b128 v[36:39], v161 offset:37888
	ds_read_b128 v[40:43], v161 offset:38912
	ds_read_b128 v[44:47], v161 offset:39936
	buffer_load_dwordx4 v222, s[36:39], s66 offen lds
	s_mov_b32 m0, s44
	s_nop 0
	buffer_load_dwordx4 v156, s[36:39], s66 offen lds
	s_waitcnt vmcnt(8)
	s_waitcnt lgkmcnt(0)
	s_barrier
	s_setprio 1
	s_waitcnt lgkmcnt(6)
	v_mfma_f32_16x16x128_f8f6f4 v[128:131], v[0:7], v[8:15], v[120:123]
	v_mfma_f32_16x16x128_f8f6f4 v[124:127], v[16:23], v[8:15], v[124:127]
	s_waitcnt lgkmcnt(4)
	v_mfma_f32_16x16x128_f8f6f4 v[108:111], v[0:7], v[24:31], v[108:111]
	v_mfma_f32_16x16x128_f8f6f4 v[104:107], v[16:23], v[24:31], v[104:107]
	s_waitcnt lgkmcnt(2)
	v_mfma_f32_16x16x128_f8f6f4 v[92:95], v[0:7], v[32:39], v[148:151]
	v_mfma_f32_16x16x128_f8f6f4 v[88:91], v[16:23], v[32:39], v[186:189]
	s_waitcnt lgkmcnt(0)
	v_mfma_f32_16x16x128_f8f6f4 v[76:79], v[0:7], v[40:47], v[218:221]
	v_mfma_f32_16x16x128_f8f6f4 v[72:75], v[16:23], v[40:47], v[226:229]
	s_setprio 0
	s_setprio 1
	v_mfma_f32_16x16x128_f8f6f4 v[116:119], v[132:139], v[8:15], v[116:119]
	v_mfma_f32_16x16x128_f8f6f4 v[112:115], v[140:147], v[8:15], v[112:115]
	v_mfma_f32_16x16x128_f8f6f4 v[100:103], v[132:139], v[24:31], v[100:103]
	v_mfma_f32_16x16x128_f8f6f4 v[96:99], v[140:147], v[24:31], v[96:99]
	v_mfma_f32_16x16x128_f8f6f4 v[84:87], v[132:139], v[32:39], v[178:181]
	v_mfma_f32_16x16x128_f8f6f4 v[80:83], v[140:147], v[32:39], v[182:185]
	v_mfma_f32_16x16x128_f8f6f4 v[68:71], v[132:139], v[40:47], v[194:197]
	v_mfma_f32_16x16x128_f8f6f4 v[64:67], v[140:147], v[40:47], v[198:201]
	s_setprio 0
	s_barrier
	s_mov_b32 m0, s45
	s_bitset1_b32 s55, 7
	ds_read_b128 v[32:35], v161 offset:49152
	ds_read_b128 v[36:39], v161 offset:50176
	ds_read_b128 v[162:165], v161 offset:51200
	ds_read_b128 v[166:169], v161 offset:52224
	ds_read_b128 v[170:173], v161 offset:53248
	ds_read_b128 v[174:177], v161 offset:54272
	ds_read_b128 v[178:181], v161 offset:55296
	ds_read_b128 v[182:185], v161 offset:56320
	buffer_load_dwordx4 v223, s[12:15], s55 offen lds
	s_mov_b32 m0, s46
	s_nop 0
	buffer_load_dwordx4 v157, s[12:15], s55 offen lds
	s_add_i32 s55, s55, s30
	s_mov_b32 m0, s52
	s_nop 0
	buffer_load_dwordx4 v223, s[12:15], s55 offen lds
	s_mov_b32 m0, s53
	s_nop 0
	buffer_load_dwordx4 v157, s[12:15], s55 offen lds
	s_mov_b32 m0, s47
	s_nop 0
	buffer_load_dwordx4 v222, s[36:39], s54 offen lds
	s_mov_b32 m0, s48
	s_nop 0
	buffer_load_dwordx4 v156, s[36:39], s54 offen lds
	s_waitcnt vmcnt(8)
	s_waitcnt lgkmcnt(0)
	s_barrier
	s_setprio 1
	s_waitcnt lgkmcnt(6)
	v_mfma_f32_16x16x128_f8f6f4 v[60:63], v[0:7], v[32:39], v[60:63]
	v_mfma_f32_16x16x128_f8f6f4 v[56:59], v[16:23], v[32:39], v[56:59]
	s_waitcnt lgkmcnt(4)
	v_mfma_f32_16x16x128_f8f6f4 v[44:47], v[0:7], v[162:169], v[202:205]
	v_mfma_f32_16x16x128_f8f6f4 v[40:43], v[16:23], v[162:169], v[206:209]
	s_waitcnt lgkmcnt(2)
	v_mfma_f32_16x16x128_f8f6f4 v[28:31], v[0:7], v[170:177], v[210:213]
	v_mfma_f32_16x16x128_f8f6f4 v[24:27], v[16:23], v[170:177], v[214:217]
	s_waitcnt lgkmcnt(0)
	v_mfma_f32_16x16x128_f8f6f4 v[12:15], v[0:7], v[178:185], v[230:233]
	v_mfma_f32_16x16x128_f8f6f4 v[8:11], v[16:23], v[178:185], v[234:237]
	s_setprio 0
	s_setprio 1
	v_mfma_f32_16x16x128_f8f6f4 v[52:55], v[132:139], v[32:39], v[52:55]
	v_mfma_f32_16x16x128_f8f6f4 v[48:51], v[140:147], v[32:39], v[48:51]
	v_mfma_f32_16x16x128_f8f6f4 v[36:39], v[132:139], v[162:169], v[238:241]
	v_mfma_f32_16x16x128_f8f6f4 v[32:35], v[140:147], v[162:169], v[242:245]
	v_mfma_f32_16x16x128_f8f6f4 v[20:23], v[132:139], v[170:177], v[246:249]
	v_mfma_f32_16x16x128_f8f6f4 v[16:19], v[140:147], v[170:177], v[250:253]
	v_mfma_f32_16x16x128_f8f6f4 v[4:7], v[132:139], v[178:185], v[190:193]
	v_mfma_f32_16x16x128_f8f6f4 v[0:3], v[140:147], v[178:185], v[152:155]
	s_setprio 0
	s_barrier
	s_add_i32 s11, s11, 2
	s_addk_i32 s4, 0x100
	s_addk_i32 s5, 0x100
	s_cmp_ge_i32 s11, s58
	s_cbranch_scc0 .LBB0_926
	v_mov_b32_e32 v230, 0x358637bd
	v_mov_b32_e32 v233, v159
	v_mov_b32_e32 v231, 1
	v_mov_b32_e32 v234, 0xff61b1e6
	s_and_b64 vcc, exec, s[24:25]
	s_cbranch_vccnz .LBB0_929
	s_branch .LBB0_930

; #define PG8_STAGE(bufoff, rs_, soff_, voff) do { _Pragma("unroll") for (int _i = 0; _i < 2; ++_i) \
;         __builtin_amdgcn_raw_ptr_buffer_load_lds(rs_, (LAS void*)(lds + (bufoff) + ldsw + _i * 8192), 16, (int)(voff)[_i], (int)(soff_), 0, 0); } while (0)
; #define PG8_LDA(dst, b, h) do { _Pragma("unroll") for (int m = 0; m < 4; ++m) dst[m] = PG8_LD2(lds + PG8_SA(b, h) + aoff + m * 2048); } while (0)
; #define PG8_LDB(dst, b, h) do { _Pragma("unroll") for (int n = 0; n < 2; ++n) dst[n] = PG8_LD2(lds + PG8_SB(b, h) + boff + n * 2048); } while (0)
; #define PG8_WAIT_V(n) asm volatile("s_waitcnt vmcnt(" #n ")" ::: "memory")
; #define PG8_WAIT_L(n) asm volatile("s_waitcnt lgkmcnt(" #n ")" ::: "memory")
; #define PG8_BAR __builtin_amdgcn_s_barrier()
; #define PG8_SCHED __builtin_amdgcn_sched_barrier(0)
; template <class Epi, class Sched, bool ALIGN_EPI = false, bool SP2 = false, bool FP8 = false>
; __device__ __forceinline__ void gemm_phase(LAS unsigned char* lds, const Gemm g, const Sched& S, const Epi& E, int wbase) {
;     ...
;             PG8_LDB(B0, 0, 0); PG8_LDB(B1, 0, 1); PG8_SCHED; PG8_LDA(At, 0, 0); PG8_STAGE(PG8_SA(1, 1), rAc, a1 + hstep, voffA);
;             PG8_WAIT_V(8); PG8_WAIT_L(0); PG8_BAR; PG8_MMA(0, 0, At, B0); PG8_MMA(0, 1, At, B1); PG8_BAR; PG8_SCHED;
;             PG8_LDA(At, 0, 1); PG8_STAGE(PG8_SB(0, 0), rB2, b2, voffB); PG8_STAGE(PG8_SB(0, 1), rB2, b2 + hstep, voffB); PG8_STAGE(PG8_SA(0, 0), rA2, a2, voffA);
.LBB0_1348:
	v_add_u32_e32 v12, 0x10000, v199
	v_add_u32_e32 v28, 0x14000, v199
	ds_read_b128 v[0:3], v12
	ds_read_b128 v[4:7], v12 offset:1024
	ds_read_b128 v[8:11], v12 offset:2048
	ds_read_b128 v[12:15], v12 offset:3072
	ds_read_b128 v[16:19], v28
	ds_read_b128 v[20:23], v28 offset:1024
	ds_read_b128 v[24:27], v28 offset:2048
	ds_read_b128 v[28:31], v28 offset:3072
	s_add_i32 s6, s67, 0x80
	s_cmp_eq_u32 s65, s85
	s_cselect_b32 s54, s66, s6
	s_cselect_b64 vcc, -1, 0
	v_cndmask_b32_e32 v211, v210, v201, vcc
	s_or_b32 s78, s54, 0x80
	s_add_i32 s6, s41, s67
	s_mov_b32 m0, s76
	ds_read_b128 v[32:35], v200
	ds_read_b128 v[36:39], v200 offset:1024
	ds_read_b128 v[40:43], v200 offset:2048
	ds_read_b128 v[44:47], v200 offset:3072
	ds_read_b128 v[48:51], v200 offset:4096
	ds_read_b128 v[52:55], v200 offset:5120
	ds_read_b128 v[56:59], v200 offset:6144
	ds_read_b128 v[60:63], v200 offset:7168
	buffer_load_dwordx4 v192, s[36:39], s6 offen lds
	s_mov_b32 m0, s77
	s_nop 0
	buffer_load_dwordx4 v195, s[36:39], s6 offen lds
	s_waitcnt vmcnt(8)
	s_waitcnt lgkmcnt(0)
	s_barrier
	s_setprio 1
	s_waitcnt lgkmcnt(6)
	v_mfma_f32_16x16x128_f8f6f4 v[184:187], v[0:7], v[32:39], v[184:187]
	v_mfma_f32_16x16x128_f8f6f4 v[188:191], v[8:15], v[32:39], v[188:191]
	s_waitcnt lgkmcnt(4)
	v_mfma_f32_16x16x128_f8f6f4 v[168:171], v[0:7], v[40:47], v[168:171]
	v_mfma_f32_16x16x128_f8f6f4 v[172:175], v[8:15], v[40:47], v[172:175]
	s_waitcnt lgkmcnt(2)
	v_mfma_f32_16x16x128_f8f6f4 v[152:155], v[0:7], v[48:55], v[152:155]
	v_mfma_f32_16x16x128_f8f6f4 v[156:159], v[8:15], v[48:55], v[156:159]
	s_waitcnt lgkmcnt(0)
	v_mfma_f32_16x16x128_f8f6f4 v[136:139], v[0:7], v[56:63], v[136:139]
	v_mfma_f32_16x16x128_f8f6f4 v[140:143], v[8:15], v[56:63], v[140:143]
	s_setprio 0
	s_setprio 1
	v_mfma_f32_16x16x128_f8f6f4 v[176:179], v[16:23], v[32:39], v[176:179]
	v_mfma_f32_16x16x128_f8f6f4 v[180:183], v[24:31], v[32:39], v[180:183]
	v_mfma_f32_16x16x128_f8f6f4 v[160:163], v[16:23], v[40:47], v[160:163]
	v_mfma_f32_16x16x128_f8f6f4 v[164:167], v[24:31], v[40:47], v[164:167]
	v_mfma_f32_16x16x128_f8f6f4 v[144:147], v[16:23], v[48:55], v[144:147]
	v_mfma_f32_16x16x128_f8f6f4 v[148:151], v[24:31], v[48:55], v[148:151]
	v_mfma_f32_16x16x128_f8f6f4 v[128:131], v[16:23], v[56:63], v[128:131]
	v_mfma_f32_16x16x128_f8f6f4 v[132:135], v[24:31], v[56:63], v[132:135]
	s_setprio 0
	s_barrier
	ds_read_b128 v[32:35], v200 offset:16384
	ds_read_b128 v[36:39], v200 offset:17408
	ds_read_b128 v[40:43], v200 offset:18432
	ds_read_b128 v[44:47], v200 offset:19456
	ds_read_b128 v[48:51], v200 offset:20480
	ds_read_b128 v[52:55], v200 offset:21504
	ds_read_b128 v[56:59], v200 offset:22528
	ds_read_b128 v[60:63], v200 offset:23552
	s_mov_b32 s6, s38
	s_mov_b32 s7, s39
	s_mov_b64 s[20:21], exec
	s_mov_b32 m0, s43

; #define PG8_STAGE(bufoff, rs_, soff_, voff) do { _Pragma("unroll") for (int _i = 0; _i < 2; ++_i) \
;         __builtin_amdgcn_raw_ptr_buffer_load_lds(rs_, (LAS void*)(lds + (bufoff) + ldsw + _i * 8192), 16, (int)(voff)[_i], (int)(soff_), 0, 0); } while (0)
; #define PG8_LDA(dst, b, h) do { _Pragma("unroll") for (int m = 0; m < 4; ++m) dst[m] = PG8_LD2(lds + PG8_SA(b, h) + aoff + m * 2048); } while (0)
; #define PG8_LDB(dst, b, h) do { _Pragma("unroll") for (int n = 0; n < 2; ++n) dst[n] = PG8_LD2(lds + PG8_SB(b, h) + boff + n * 2048); } while (0)
; #define PG8_WAIT_V(n) asm volatile("s_waitcnt vmcnt(" #n ")" ::: "memory")
; #define PG8_WAIT_L(n) asm volatile("s_waitcnt lgkmcnt(" #n ")" ::: "memory")
; #define PG8_BAR __builtin_amdgcn_s_barrier()
; #define PG8_SCHED __builtin_amdgcn_sched_barrier(0)
; template <class Epi, class Sched, bool ALIGN_EPI = false, bool SP2 = false, bool FP8 = false>
; __device__ __forceinline__ void gemm_phase(LAS unsigned char* lds, const Gemm g, const Sched& S, const Epi& E, int wbase) {
;     ...
;             PG8_LDA(At, 0, 1); PG8_STAGE(PG8_SB(0, 0), rB2, b2, voffB); PG8_STAGE(PG8_SB(0, 1), rB2, b2 + hstep, voffB); PG8_STAGE(PG8_SA(0, 0), rA2, a2, voffA);
;             PG8_WAIT_V(8); PG8_WAIT_L(0); PG8_BAR; PG8_MMA(1, 0, At, B0); PG8_MMA(1, 1, At, B1); PG8_BAR; PG8_SCHED;
;             PG8_LDB(B0, 1, 0); PG8_LDB(B1, 1, 1); PG8_SCHED; PG8_LDA(At, 1, 0); PG8_STAGE(PG8_SA(0, 1), rA2, a2 + hstep, voffA);
;             PG8_WAIT_V(8); PG8_WAIT_L(0); PG8_BAR; PG8_MMA(0, 0, At, B0); PG8_MMA(0, 1, At, B1); PG8_BAR; PG8_SCHED;
;             PG8_LDA(At, 1, 1); PG8_STAGE(PG8_SB(1, 0), rB2, b3, voffB); PG8_STAGE(PG8_SB(1, 1), rB2, b3 + hstep, voffB); PG8_STAGE(PG8_SA(1, 0), rA2, a3, voffA);
.LBB0_1355:
	v_readfirstlane_b32 s55, v212
	s_nop 1
	v_cmp_eq_u32_e32 vcc, s55, v212
	s_and_saveexec_b64 vcc, vcc
	s_nop 0
	buffer_load_dwordx4 v196, s[4:7], s55 offen lds
	s_xor_b64 exec, exec, vcc
	s_cbranch_execnz .LBB0_1355
	s_mov_b64 exec, s[20:21]
	s_mov_b32 m0, s42
	s_nop 0
	buffer_load_dwordx4 v192, s[36:39], s54 offen lds
	s_mov_b32 m0, s47
	s_nop 0
	buffer_load_dwordx4 v195, s[36:39], s54 offen lds
	s_waitcnt vmcnt(8)
	s_waitcnt lgkmcnt(0)
	s_barrier
	s_setprio 1
	s_waitcnt lgkmcnt(6)
	v_mfma_f32_16x16x128_f8f6f4 v[120:123], v[0:7], v[32:39], v[120:123]
	v_mfma_f32_16x16x128_f8f6f4 v[124:127], v[8:15], v[32:39], v[124:127]
	s_waitcnt lgkmcnt(4)
	v_mfma_f32_16x16x128_f8f6f4 v[104:107], v[0:7], v[40:47], v[104:107]
	v_mfma_f32_16x16x128_f8f6f4 v[108:111], v[8:15], v[40:47], v[108:111]
	s_waitcnt lgkmcnt(2)
	v_mfma_f32_16x16x128_f8f6f4 v[88:91], v[0:7], v[48:55], v[88:91]
	v_mfma_f32_16x16x128_f8f6f4 v[92:95], v[8:15], v[48:55], v[92:95]
	s_waitcnt lgkmcnt(0)
	v_mfma_f32_16x16x128_f8f6f4 v[72:75], v[0:7], v[56:63], v[72:75]
	v_mfma_f32_16x16x128_f8f6f4 v[76:79], v[8:15], v[56:63], v[76:79]
	s_setprio 0
	s_setprio 1
	v_mfma_f32_16x16x128_f8f6f4 v[112:115], v[16:23], v[32:39], v[112:115]
	v_mfma_f32_16x16x128_f8f6f4 v[116:119], v[24:31], v[32:39], v[116:119]
	v_mfma_f32_16x16x128_f8f6f4 v[96:99], v[16:23], v[40:47], v[96:99]
	v_mfma_f32_16x16x128_f8f6f4 v[100:103], v[24:31], v[40:47], v[100:103]
	v_mfma_f32_16x16x128_f8f6f4 v[80:83], v[16:23], v[48:55], v[80:83]
	v_mfma_f32_16x16x128_f8f6f4 v[84:87], v[24:31], v[48:55], v[84:87]
	v_mfma_f32_16x16x128_f8f6f4 v[68:71], v[16:23], v[56:63], v[68:71]
	v_mfma_f32_16x16x128_f8f6f4 v[64:67], v[24:31], v[56:63], v[64:67]
	s_setprio 0
	s_barrier
	v_add_u32_e32 v12, 0x18000, v199
	v_add_u32_e32 v28, 0x1c000, v199
	ds_read_b128 v[0:3], v12
	ds_read_b128 v[4:7], v12 offset:1024
	ds_read_b128 v[8:11], v12 offset:2048
	ds_read_b128 v[12:15], v12 offset:3072
	ds_read_b128 v[16:19], v28
	ds_read_b128 v[20:23], v28 offset:1024
	ds_read_b128 v[24:27], v28 offset:2048
	ds_read_b128 v[28:31], v28 offset:3072
	s_add_i32 s54, s54, s41
	s_mov_b32 m0, s48
	ds_read_b128 v[32:35], v200 offset:32768
	ds_read_b128 v[36:39], v200 offset:33792
	ds_read_b128 v[40:43], v200 offset:34816
	ds_read_b128 v[44:47], v200 offset:35840
	ds_read_b128 v[48:51], v200 offset:36864
	ds_read_b128 v[52:55], v200 offset:37888
	ds_read_b128 v[56:59], v200 offset:38912
	ds_read_b128 v[60:63], v200 offset:39936
	buffer_load_dwordx4 v192, s[36:39], s54 offen lds
	s_mov_b32 m0, s52
	s_nop 0
	buffer_load_dwordx4 v195, s[36:39], s54 offen lds
	s_waitcnt vmcnt(8)
	s_waitcnt lgkmcnt(0)
	s_barrier
	s_setprio 1
	s_waitcnt lgkmcnt(6)
	v_mfma_f32_16x16x128_f8f6f4 v[184:187], v[0:7], v[32:39], v[184:187]
	v_mfma_f32_16x16x128_f8f6f4 v[188:191], v[8:15], v[32:39], v[188:191]
	s_waitcnt lgkmcnt(4)
	v_mfma_f32_16x16x128_f8f6f4 v[168:171], v[0:7], v[40:47], v[168:171]
	v_mfma_f32_16x16x128_f8f6f4 v[172:175], v[8:15], v[40:47], v[172:175]
	s_waitcnt lgkmcnt(2)
	v_mfma_f32_16x16x128_f8f6f4 v[152:155], v[0:7], v[48:55], v[152:155]
	v_mfma_f32_16x16x128_f8f6f4 v[156:159], v[8:15], v[48:55], v[156:159]
	s_waitcnt lgkmcnt(0)
	v_mfma_f32_16x16x128_f8f6f4 v[136:139], v[0:7], v[56:63], v[136:139]
	v_mfma_f32_16x16x128_f8f6f4 v[140:143], v[8:15], v[56:63], v[140:143]
	s_setprio 0
	s_setprio 1
	v_mfma_f32_16x16x128_f8f6f4 v[176:179], v[16:23], v[32:39], v[176:179]
	v_mfma_f32_16x16x128_f8f6f4 v[180:183], v[24:31], v[32:39], v[180:183]
	v_mfma_f32_16x16x128_f8f6f4 v[160:163], v[16:23], v[40:47], v[160:163]
	v_mfma_f32_16x16x128_f8f6f4 v[164:167], v[24:31], v[40:47], v[164:167]
	v_mfma_f32_16x16x128_f8f6f4 v[144:147], v[16:23], v[48:55], v[144:147]
	v_mfma_f32_16x16x128_f8f6f4 v[148:151], v[24:31], v[48:55], v[148:151]
	v_mfma_f32_16x16x128_f8f6f4 v[128:131], v[16:23], v[56:63], v[128:131]
	v_mfma_f32_16x16x128_f8f6f4 v[132:135], v[24:31], v[56:63], v[132:135]
	s_setprio 0
	s_barrier
	ds_read_b128 v[32:35], v200 offset:49152
	ds_read_b128 v[36:39], v200 offset:50176
	ds_read_b128 v[40:43], v200 offset:51200
	ds_read_b128 v[44:47], v200 offset:52224
	ds_read_b128 v[48:51], v200 offset:53248
	ds_read_b128 v[52:55], v200 offset:54272
	ds_read_b128 v[56:59], v200 offset:55296
	ds_read_b128 v[60:63], v200 offset:56320
	v_add_u32_e32 v211, 0x80, v211
	s_mov_b64 s[20:21], exec
	s_mov_b32 m0, s57

; #define PG8_STAGE(bufoff, rs_, soff_, voff) do { _Pragma("unroll") for (int _i = 0; _i < 2; ++_i) \
;         __builtin_amdgcn_raw_ptr_buffer_load_lds(rs_, (LAS void*)(lds + (bufoff) + ldsw + _i * 8192), 16, (int)(voff)[_i], (int)(soff_), 0, 0); } while (0)
; #define PG8_LDA(dst, b, h) do { _Pragma("unroll") for (int m = 0; m < 4; ++m) dst[m] = PG8_LD2(lds + PG8_SA(b, h) + aoff + m * 2048); } while (0)
; #define PG8_WAIT_V(n) asm volatile("s_waitcnt vmcnt(" #n ")" ::: "memory")
; #define PG8_WAIT_L(n) asm volatile("s_waitcnt lgkmcnt(" #n ")" ::: "memory")
; #define PG8_BAR __builtin_amdgcn_s_barrier()
; #define PG8_SCHED __builtin_amdgcn_sched_barrier(0)
; template <class Epi, class Sched, bool ALIGN_EPI = false, bool SP2 = false, bool FP8 = false>
; __device__ __forceinline__ void gemm_phase(LAS unsigned char* lds, const Gemm g, const Sched& S, const Epi& E, int wbase) {
;     ...
;             PG8_LDA(At, 1, 1); PG8_STAGE(PG8_SB(1, 0), rB2, b3, voffB); PG8_STAGE(PG8_SB(1, 1), rB2, b3 + hstep, voffB); PG8_STAGE(PG8_SA(1, 0), rA2, a3, voffA);
;             PG8_WAIT_V(8); PG8_WAIT_L(0); PG8_BAR; PG8_MMA(1, 0, At, B0); PG8_MMA(1, 1, At, B1); PG8_BAR; PG8_SCHED;
.LBB0_1363:
	v_readfirstlane_b32 s54, v211
	s_nop 1
	v_cmp_eq_u32_e32 vcc, s54, v211
	s_and_saveexec_b64 vcc, vcc
	s_nop 0
	buffer_load_dwordx4 v196, s[4:7], s54 offen lds
	s_xor_b64 exec, exec, vcc
	s_cbranch_execnz .LBB0_1363
	s_mov_b64 exec, s[20:21]
	s_mov_b32 m0, s59
	s_nop 0
	buffer_load_dwordx4 v192, s[36:39], s78 offen lds
	s_mov_b32 m0, s60
	s_nop 0
	buffer_load_dwordx4 v195, s[36:39], s78 offen lds
	s_waitcnt vmcnt(8)
	s_waitcnt lgkmcnt(0)
	s_barrier
	s_setprio 1
	s_waitcnt lgkmcnt(6)
	v_mfma_f32_16x16x128_f8f6f4 v[120:123], v[0:7], v[32:39], v[120:123]
	v_mfma_f32_16x16x128_f8f6f4 v[124:127], v[8:15], v[32:39], v[124:127]
	s_waitcnt lgkmcnt(4)
	v_mfma_f32_16x16x128_f8f6f4 v[104:107], v[0:7], v[40:47], v[104:107]
	v_mfma_f32_16x16x128_f8f6f4 v[108:111], v[8:15], v[40:47], v[108:111]
	s_waitcnt lgkmcnt(2)
	v_mfma_f32_16x16x128_f8f6f4 v[88:91], v[0:7], v[48:55], v[88:91]
	v_mfma_f32_16x16x128_f8f6f4 v[92:95], v[8:15], v[48:55], v[92:95]
	s_waitcnt lgkmcnt(0)
	v_mfma_f32_16x16x128_f8f6f4 v[72:75], v[0:7], v[56:63], v[72:75]
	v_mfma_f32_16x16x128_f8f6f4 v[76:79], v[8:15], v[56:63], v[76:79]
	s_setprio 0
	s_setprio 1
	v_mfma_f32_16x16x128_f8f6f4 v[112:115], v[16:23], v[32:39], v[112:115]
	v_mfma_f32_16x16x128_f8f6f4 v[116:119], v[24:31], v[32:39], v[116:119]
	v_mfma_f32_16x16x128_f8f6f4 v[96:99], v[16:23], v[40:47], v[96:99]
	v_mfma_f32_16x16x128_f8f6f4 v[100:103], v[24:31], v[40:47], v[100:103]
	v_mfma_f32_16x16x128_f8f6f4 v[80:83], v[16:23], v[48:55], v[80:83]
	v_mfma_f32_16x16x128_f8f6f4 v[84:87], v[24:31], v[48:55], v[84:87]
	v_mfma_f32_16x16x128_f8f6f4 v[68:71], v[16:23], v[56:63], v[68:71]
	v_mfma_f32_16x16x128_f8f6f4 v[64:67], v[24:31], v[56:63], v[64:67]
	s_setprio 0
	s_barrier
	s_add_i32 s85, s85, 2
	s_addk_i32 s67, 0x100
	s_cmp_ge_i32 s85, s53
	v_add_u32_e32 v210, 0x100, v210
	s_cbranch_scc0 .LBB0_1348
	v_readlane_b32 s54, v255, 25
	v_readlane_b32 s55, v255, 26
	s_and_b64 vcc, exec, s[18:19]
	s_cbranch_vccnz .LBB0_1367
	s_branch .LBB0_1368

; #define PG8_STAGE(bufoff, rs_, soff_, voff) do { _Pragma("unroll") for (int _i = 0; _i < 2; ++_i) \
;         __builtin_amdgcn_raw_ptr_buffer_load_lds(rs_, (LAS void*)(lds + (bufoff) + ldsw + _i * 8192), 16, (int)(voff)[_i], (int)(soff_), 0, 0); } while (0)
; #define PG8_LDA(dst, b, h) do { _Pragma("unroll") for (int m = 0; m < 4; ++m) dst[m] = PG8_LD2(lds + PG8_SA(b, h) + aoff + m * 2048); } while (0)
; #define PG8_LDB(dst, b, h) do { _Pragma("unroll") for (int n = 0; n < 2; ++n) dst[n] = PG8_LD2(lds + PG8_SB(b, h) + boff + n * 2048); } while (0)
; #define PG8_WAIT_V(n) asm volatile("s_waitcnt vmcnt(" #n ")" ::: "memory")
; #define PG8_WAIT_L(n) asm volatile("s_waitcnt lgkmcnt(" #n ")" ::: "memory")
; #define PG8_BAR __builtin_amdgcn_s_barrier()
; #define PG8_SCHED __builtin_amdgcn_sched_barrier(0)
; template <class Epi, class Sched, bool ALIGN_EPI = false, bool SP2 = false, bool FP8 = false>
; __device__ __forceinline__ void gemm_phase(LAS unsigned char* lds, const Gemm g, const Sched& S, const Epi& E, int wbase) {
;     ...
;             PG8_LDB(B0, 0, 0); PG8_LDB(B1, 0, 1); PG8_SCHED; PG8_LDA(At, 0, 0); PG8_STAGE(PG8_SA(1, 1), rAc, a1 + hstep, voffA);
;             PG8_WAIT_V(8); PG8_WAIT_L(0); PG8_BAR; PG8_MMA(0, 0, At, B0); PG8_MMA(0, 1, At, B1); PG8_BAR; PG8_SCHED;
;             PG8_LDA(At, 0, 1); PG8_STAGE(PG8_SB(0, 0), rB2, b2, voffB); PG8_STAGE(PG8_SB(0, 1), rB2, b2 + hstep, voffB); PG8_STAGE(PG8_SA(0, 0), rA2, a2, voffA);
.LBB0_1453:
	v_add_u32_e32 v12, 0x10000, v199
	v_add_u32_e32 v28, 0x14000, v199
	ds_read_b128 v[0:3], v12
	ds_read_b128 v[4:7], v12 offset:1024
	ds_read_b128 v[8:11], v12 offset:2048
	ds_read_b128 v[12:15], v12 offset:3072
	ds_read_b128 v[16:19], v28
	ds_read_b128 v[20:23], v28 offset:1024
	ds_read_b128 v[24:27], v28 offset:2048
	ds_read_b128 v[28:31], v28 offset:3072
	s_add_i32 s6, s67, 0x80
	s_cmp_eq_u32 s61, s81
	s_cselect_b32 s54, s66, s6
	s_cselect_b64 vcc, -1, 0
	v_cndmask_b32_e32 v203, v202, v201, vcc
	s_or_b32 s78, s54, 0x80
	s_add_i32 s6, s34, s67
	s_mov_b32 m0, s62
	ds_read_b128 v[32:35], v200
	ds_read_b128 v[36:39], v200 offset:1024
	ds_read_b128 v[40:43], v200 offset:2048
	ds_read_b128 v[44:47], v200 offset:3072
	ds_read_b128 v[48:51], v200 offset:4096
	ds_read_b128 v[52:55], v200 offset:5120
	ds_read_b128 v[56:59], v200 offset:6144
	ds_read_b128 v[60:63], v200 offset:7168
	buffer_load_dwordx4 v192, s[36:39], s6 offen lds
	s_mov_b32 m0, s63
	s_nop 0
	buffer_load_dwordx4 v195, s[36:39], s6 offen lds
	s_waitcnt vmcnt(8)
	s_waitcnt lgkmcnt(0)
	s_barrier
	s_setprio 1
	s_waitcnt lgkmcnt(6)
	v_mfma_f32_16x16x128_f8f6f4 v[188:191], v[0:7], v[32:39], v[188:191]
	v_mfma_f32_16x16x128_f8f6f4 v[184:187], v[8:15], v[32:39], v[184:187]
	s_waitcnt lgkmcnt(4)
	v_mfma_f32_16x16x128_f8f6f4 v[172:175], v[0:7], v[40:47], v[172:175]
	v_mfma_f32_16x16x128_f8f6f4 v[168:171], v[8:15], v[40:47], v[168:171]
	s_waitcnt lgkmcnt(2)
	v_mfma_f32_16x16x128_f8f6f4 v[156:159], v[0:7], v[48:55], v[156:159]
	v_mfma_f32_16x16x128_f8f6f4 v[152:155], v[8:15], v[48:55], v[152:155]
	s_waitcnt lgkmcnt(0)
	v_mfma_f32_16x16x128_f8f6f4 v[140:143], v[0:7], v[56:63], v[140:143]
	v_mfma_f32_16x16x128_f8f6f4 v[136:139], v[8:15], v[56:63], v[136:139]
	s_setprio 0
	s_setprio 1
	v_mfma_f32_16x16x128_f8f6f4 v[180:183], v[16:23], v[32:39], v[180:183]
	v_mfma_f32_16x16x128_f8f6f4 v[176:179], v[24:31], v[32:39], v[176:179]
	v_mfma_f32_16x16x128_f8f6f4 v[164:167], v[16:23], v[40:47], v[164:167]
	v_mfma_f32_16x16x128_f8f6f4 v[160:163], v[24:31], v[40:47], v[160:163]
	v_mfma_f32_16x16x128_f8f6f4 v[148:151], v[16:23], v[48:55], v[148:151]
	v_mfma_f32_16x16x128_f8f6f4 v[144:147], v[24:31], v[48:55], v[144:147]
	v_mfma_f32_16x16x128_f8f6f4 v[132:135], v[16:23], v[56:63], v[132:135]
	v_mfma_f32_16x16x128_f8f6f4 v[128:131], v[24:31], v[56:63], v[128:131]
	s_setprio 0
	s_barrier
	ds_read_b128 v[32:35], v200 offset:16384
	ds_read_b128 v[36:39], v200 offset:17408
	ds_read_b128 v[40:43], v200 offset:18432
	ds_read_b128 v[44:47], v200 offset:19456
	ds_read_b128 v[48:51], v200 offset:20480
	ds_read_b128 v[52:55], v200 offset:21504
	ds_read_b128 v[56:59], v200 offset:22528
	ds_read_b128 v[60:63], v200 offset:23552
	s_mov_b32 s6, s38
	s_mov_b32 s7, s39
	s_mov_b64 s[18:19], exec
	s_mov_b32 m0, s41

; #define PG8_STAGE(bufoff, rs_, soff_, voff) do { _Pragma("unroll") for (int _i = 0; _i < 2; ++_i) \
;         __builtin_amdgcn_raw_ptr_buffer_load_lds(rs_, (LAS void*)(lds + (bufoff) + ldsw + _i * 8192), 16, (int)(voff)[_i], (int)(soff_), 0, 0); } while (0)
; #define PG8_LDA(dst, b, h) do { _Pragma("unroll") for (int m = 0; m < 4; ++m) dst[m] = PG8_LD2(lds + PG8_SA(b, h) + aoff + m * 2048); } while (0)
; #define PG8_LDB(dst, b, h) do { _Pragma("unroll") for (int n = 0; n < 2; ++n) dst[n] = PG8_LD2(lds + PG8_SB(b, h) + boff + n * 2048); } while (0)
; #define PG8_WAIT_V(n) asm volatile("s_waitcnt vmcnt(" #n ")" ::: "memory")
; #define PG8_WAIT_L(n) asm volatile("s_waitcnt lgkmcnt(" #n ")" ::: "memory")
; #define PG8_BAR __builtin_amdgcn_s_barrier()
; #define PG8_SCHED __builtin_amdgcn_sched_barrier(0)
; template <class Epi, class Sched, bool ALIGN_EPI = false, bool SP2 = false, bool FP8 = false>
; __device__ __forceinline__ void gemm_phase(LAS unsigned char* lds, const Gemm g, const Sched& S, const Epi& E, int wbase) {
;     ...
;             PG8_LDA(At, 0, 1); PG8_STAGE(PG8_SB(0, 0), rB2, b2, voffB); PG8_STAGE(PG8_SB(0, 1), rB2, b2 + hstep, voffB); PG8_STAGE(PG8_SA(0, 0), rA2, a2, voffA);
;             PG8_WAIT_V(8); PG8_WAIT_L(0); PG8_BAR; PG8_MMA(1, 0, At, B0); PG8_MMA(1, 1, At, B1); PG8_BAR; PG8_SCHED;
;             PG8_LDB(B0, 1, 0); PG8_LDB(B1, 1, 1); PG8_SCHED; PG8_LDA(At, 1, 0); PG8_STAGE(PG8_SA(0, 1), rA2, a2 + hstep, voffA);
;             PG8_WAIT_V(8); PG8_WAIT_L(0); PG8_BAR; PG8_MMA(0, 0, At, B0); PG8_MMA(0, 1, At, B1); PG8_BAR; PG8_SCHED;
;             PG8_LDA(At, 1, 1); PG8_STAGE(PG8_SB(1, 0), rB2, b3, voffB); PG8_STAGE(PG8_SB(1, 1), rB2, b3 + hstep, voffB); PG8_STAGE(PG8_SA(1, 0), rA2, a3, voffA);
.LBB0_1460:
	v_readfirstlane_b32 s55, v204
	s_nop 1
	v_cmp_eq_u32_e32 vcc, s55, v204
	s_and_saveexec_b64 vcc, vcc
	s_nop 0
	buffer_load_dwordx4 v196, s[4:7], s55 offen lds
	s_xor_b64 exec, exec, vcc
	s_cbranch_execnz .LBB0_1460
	s_mov_b64 exec, s[18:19]
	s_mov_b32 m0, s35
	s_nop 0
	buffer_load_dwordx4 v192, s[36:39], s54 offen lds
	s_mov_b32 m0, s45
	s_nop 0
	buffer_load_dwordx4 v195, s[36:39], s54 offen lds
	s_waitcnt vmcnt(8)
	s_waitcnt lgkmcnt(0)
	s_barrier
	s_setprio 1
	s_waitcnt lgkmcnt(6)
	v_mfma_f32_16x16x128_f8f6f4 v[124:127], v[0:7], v[32:39], v[124:127]
	v_mfma_f32_16x16x128_f8f6f4 v[120:123], v[8:15], v[32:39], v[120:123]
	s_waitcnt lgkmcnt(4)
	v_mfma_f32_16x16x128_f8f6f4 v[108:111], v[0:7], v[40:47], v[108:111]
	v_mfma_f32_16x16x128_f8f6f4 v[104:107], v[8:15], v[40:47], v[104:107]
	s_waitcnt lgkmcnt(2)
	v_mfma_f32_16x16x128_f8f6f4 v[92:95], v[0:7], v[48:55], v[92:95]
	v_mfma_f32_16x16x128_f8f6f4 v[88:91], v[8:15], v[48:55], v[88:91]
	s_waitcnt lgkmcnt(0)
	v_mfma_f32_16x16x128_f8f6f4 v[76:79], v[0:7], v[56:63], v[76:79]
	v_mfma_f32_16x16x128_f8f6f4 v[72:75], v[8:15], v[56:63], v[72:75]
	s_setprio 0
	s_setprio 1
	v_mfma_f32_16x16x128_f8f6f4 v[116:119], v[16:23], v[32:39], v[116:119]
	v_mfma_f32_16x16x128_f8f6f4 v[112:115], v[24:31], v[32:39], v[112:115]
	v_mfma_f32_16x16x128_f8f6f4 v[100:103], v[16:23], v[40:47], v[100:103]
	v_mfma_f32_16x16x128_f8f6f4 v[96:99], v[24:31], v[40:47], v[96:99]
	v_mfma_f32_16x16x128_f8f6f4 v[84:87], v[16:23], v[48:55], v[84:87]
	v_mfma_f32_16x16x128_f8f6f4 v[80:83], v[24:31], v[48:55], v[80:83]
	v_mfma_f32_16x16x128_f8f6f4 v[68:71], v[16:23], v[56:63], v[68:71]
	v_mfma_f32_16x16x128_f8f6f4 v[64:67], v[24:31], v[56:63], v[64:67]
	s_setprio 0
	s_barrier
	v_add_u32_e32 v12, 0x18000, v199
	v_add_u32_e32 v28, 0x1c000, v199
	ds_read_b128 v[0:3], v12
	ds_read_b128 v[4:7], v12 offset:1024
	ds_read_b128 v[8:11], v12 offset:2048
	ds_read_b128 v[12:15], v12 offset:3072
	ds_read_b128 v[16:19], v28
	ds_read_b128 v[20:23], v28 offset:1024
	ds_read_b128 v[24:27], v28 offset:2048
	ds_read_b128 v[28:31], v28 offset:3072
	s_add_i32 s54, s54, s34
	s_mov_b32 m0, s46
	ds_read_b128 v[32:35], v200 offset:32768
	ds_read_b128 v[36:39], v200 offset:33792
	ds_read_b128 v[40:43], v200 offset:34816
	ds_read_b128 v[44:47], v200 offset:35840
	ds_read_b128 v[48:51], v200 offset:36864
	ds_read_b128 v[52:55], v200 offset:37888
	ds_read_b128 v[56:59], v200 offset:38912
	ds_read_b128 v[60:63], v200 offset:39936
	buffer_load_dwordx4 v192, s[36:39], s54 offen lds
	s_mov_b32 m0, s47
	s_nop 0
	buffer_load_dwordx4 v195, s[36:39], s54 offen lds
	s_waitcnt vmcnt(8)
	s_waitcnt lgkmcnt(0)
	s_barrier
	s_setprio 1
	s_waitcnt lgkmcnt(6)
	v_mfma_f32_16x16x128_f8f6f4 v[188:191], v[0:7], v[32:39], v[188:191]
	v_mfma_f32_16x16x128_f8f6f4 v[184:187], v[8:15], v[32:39], v[184:187]
	s_waitcnt lgkmcnt(4)
	v_mfma_f32_16x16x128_f8f6f4 v[172:175], v[0:7], v[40:47], v[172:175]
	v_mfma_f32_16x16x128_f8f6f4 v[168:171], v[8:15], v[40:47], v[168:171]
	s_waitcnt lgkmcnt(2)
	v_mfma_f32_16x16x128_f8f6f4 v[156:159], v[0:7], v[48:55], v[156:159]
	v_mfma_f32_16x16x128_f8f6f4 v[152:155], v[8:15], v[48:55], v[152:155]
	s_waitcnt lgkmcnt(0)
	v_mfma_f32_16x16x128_f8f6f4 v[140:143], v[0:7], v[56:63], v[140:143]
	v_mfma_f32_16x16x128_f8f6f4 v[136:139], v[8:15], v[56:63], v[136:139]
	s_setprio 0
	s_setprio 1
	v_mfma_f32_16x16x128_f8f6f4 v[180:183], v[16:23], v[32:39], v[180:183]
	v_mfma_f32_16x16x128_f8f6f4 v[176:179], v[24:31], v[32:39], v[176:179]
	v_mfma_f32_16x16x128_f8f6f4 v[164:167], v[16:23], v[40:47], v[164:167]
	v_mfma_f32_16x16x128_f8f6f4 v[160:163], v[24:31], v[40:47], v[160:163]
	v_mfma_f32_16x16x128_f8f6f4 v[148:151], v[16:23], v[48:55], v[148:151]
	v_mfma_f32_16x16x128_f8f6f4 v[144:147], v[24:31], v[48:55], v[144:147]
	v_mfma_f32_16x16x128_f8f6f4 v[132:135], v[16:23], v[56:63], v[132:135]
	v_mfma_f32_16x16x128_f8f6f4 v[128:131], v[24:31], v[56:63], v[128:131]
	s_setprio 0
	s_barrier
	ds_read_b128 v[32:35], v200 offset:49152
	ds_read_b128 v[36:39], v200 offset:50176
	ds_read_b128 v[40:43], v200 offset:51200
	ds_read_b128 v[44:47], v200 offset:52224
	ds_read_b128 v[48:51], v200 offset:53248
	ds_read_b128 v[52:55], v200 offset:54272
	ds_read_b128 v[56:59], v200 offset:55296
	ds_read_b128 v[60:63], v200 offset:56320
	v_add_u32_e32 v203, 0x80, v203
	s_mov_b64 s[18:19], exec
	s_mov_b32 m0, s53

; #define PG8_STAGE(bufoff, rs_, soff_, voff) do { _Pragma("unroll") for (int _i = 0; _i < 2; ++_i) \
;         __builtin_amdgcn_raw_ptr_buffer_load_lds(rs_, (LAS void*)(lds + (bufoff) + ldsw + _i * 8192), 16, (int)(voff)[_i], (int)(soff_), 0, 0); } while (0)
; #define PG8_LDA(dst, b, h) do { _Pragma("unroll") for (int m = 0; m < 4; ++m) dst[m] = PG8_LD2(lds + PG8_SA(b, h) + aoff + m * 2048); } while (0)
; #define PG8_WAIT_V(n) asm volatile("s_waitcnt vmcnt(" #n ")" ::: "memory")
; #define PG8_WAIT_L(n) asm volatile("s_waitcnt lgkmcnt(" #n ")" ::: "memory")
; #define PG8_BAR __builtin_amdgcn_s_barrier()
; #define PG8_SCHED __builtin_amdgcn_sched_barrier(0)
; template <class Epi, class Sched, bool ALIGN_EPI = false, bool SP2 = false, bool FP8 = false>
; __device__ __forceinline__ void gemm_phase(LAS unsigned char* lds, const Gemm g, const Sched& S, const Epi& E, int wbase) {
;     ...
;             PG8_LDA(At, 1, 1); PG8_STAGE(PG8_SB(1, 0), rB2, b3, voffB); PG8_STAGE(PG8_SB(1, 1), rB2, b3 + hstep, voffB); PG8_STAGE(PG8_SA(1, 0), rA2, a3, voffA);
;             PG8_WAIT_V(8); PG8_WAIT_L(0); PG8_BAR; PG8_MMA(1, 0, At, B0); PG8_MMA(1, 1, At, B1); PG8_BAR; PG8_SCHED;
.LBB0_1468:
	v_readfirstlane_b32 s54, v203
	s_nop 1
	v_cmp_eq_u32_e32 vcc, s54, v203
	s_and_saveexec_b64 vcc, vcc
	s_nop 0
	buffer_load_dwordx4 v196, s[4:7], s54 offen lds
	s_xor_b64 exec, exec, vcc
	s_cbranch_execnz .LBB0_1468
	s_mov_b64 exec, s[18:19]
	s_mov_b32 m0, s57
	s_nop 0
	buffer_load_dwordx4 v192, s[36:39], s78 offen lds
	s_mov_b32 m0, s58
	s_nop 0
	buffer_load_dwordx4 v195, s[36:39], s78 offen lds
	s_waitcnt vmcnt(8)
	s_waitcnt lgkmcnt(0)
	s_barrier
	s_setprio 1
	s_waitcnt lgkmcnt(6)
	v_mfma_f32_16x16x128_f8f6f4 v[124:127], v[0:7], v[32:39], v[124:127]
	v_mfma_f32_16x16x128_f8f6f4 v[120:123], v[8:15], v[32:39], v[120:123]
	s_waitcnt lgkmcnt(4)
	v_mfma_f32_16x16x128_f8f6f4 v[108:111], v[0:7], v[40:47], v[108:111]
	v_mfma_f32_16x16x128_f8f6f4 v[104:107], v[8:15], v[40:47], v[104:107]
	s_waitcnt lgkmcnt(2)
	v_mfma_f32_16x16x128_f8f6f4 v[92:95], v[0:7], v[48:55], v[92:95]
	v_mfma_f32_16x16x128_f8f6f4 v[88:91], v[8:15], v[48:55], v[88:91]
	s_waitcnt lgkmcnt(0)
	v_mfma_f32_16x16x128_f8f6f4 v[76:79], v[0:7], v[56:63], v[76:79]
	v_mfma_f32_16x16x128_f8f6f4 v[72:75], v[8:15], v[56:63], v[72:75]
	s_setprio 0
	s_setprio 1
	v_mfma_f32_16x16x128_f8f6f4 v[116:119], v[16:23], v[32:39], v[116:119]
	v_mfma_f32_16x16x128_f8f6f4 v[112:115], v[24:31], v[32:39], v[112:115]
	v_mfma_f32_16x16x128_f8f6f4 v[100:103], v[16:23], v[40:47], v[100:103]
	v_mfma_f32_16x16x128_f8f6f4 v[96:99], v[24:31], v[40:47], v[96:99]
	v_mfma_f32_16x16x128_f8f6f4 v[84:87], v[16:23], v[48:55], v[84:87]
	v_mfma_f32_16x16x128_f8f6f4 v[80:83], v[24:31], v[48:55], v[80:83]
	v_mfma_f32_16x16x128_f8f6f4 v[68:71], v[16:23], v[56:63], v[68:71]
	v_mfma_f32_16x16x128_f8f6f4 v[64:67], v[24:31], v[56:63], v[64:67]
	s_setprio 0
	s_barrier
	s_add_i32 s81, s81, 2
	s_addk_i32 s67, 0x100
	s_cmp_ge_i32 s81, s48
	v_add_u32_e32 v202, 0x100, v202
	s_cbranch_scc0 .LBB0_1453
	v_readlane_b32 s54, v255, 25
	v_readlane_b32 s55, v255, 26
	s_and_b64 vcc, exec, s[14:15]
	s_cbranch_vccnz .LBB0_1472
	s_branch .LBB0_1473

; #define PG8_STAGE(bufoff, rs_, soff_, voff) do { _Pragma("unroll") for (int _i = 0; _i < 2; ++_i) \
;         __builtin_amdgcn_raw_ptr_buffer_load_lds(rs_, (LAS void*)(lds + (bufoff) + ldsw + _i * 8192), 16, (int)(voff)[_i], (int)(soff_), 0, 0); } while (0)
; #define PG8_LDA(dst, b, h) do { _Pragma("unroll") for (int m = 0; m < 4; ++m) dst[m] = PG8_LD2(lds + PG8_SA(b, h) + aoff + m * 2048); } while (0)
; #define PG8_LDB(dst, b, h) do { _Pragma("unroll") for (int n = 0; n < 2; ++n) dst[n] = PG8_LD2(lds + PG8_SB(b, h) + boff + n * 2048); } while (0)
; #define PG8_WAIT_V(n) asm volatile("s_waitcnt vmcnt(" #n ")" ::: "memory")
; #define PG8_WAIT_L(n) asm volatile("s_waitcnt lgkmcnt(" #n ")" ::: "memory")
; #define PG8_BAR __builtin_amdgcn_s_barrier()
; #define PG8_SCHED __builtin_amdgcn_sched_barrier(0)
; template <class Epi, class Sched, bool ALIGN_EPI = false, bool SP2 = false, bool FP8 = false>
; __device__ __forceinline__ void gemm_phase(LAS unsigned char* lds, const Gemm g, const Sched& S, const Epi& E, int wbase) {
;     ...
;             PG8_LDB(B0, 0, 0); PG8_LDB(B1, 0, 1); PG8_SCHED; PG8_LDA(At, 0, 0); PG8_STAGE(PG8_SA(1, 1), rAc, a1 + hstep, voffA);
;             PG8_WAIT_V(8); PG8_WAIT_L(0); PG8_BAR; PG8_MMA(0, 0, At, B0); PG8_MMA(0, 1, At, B1); PG8_BAR; PG8_SCHED;
;             PG8_LDA(At, 0, 1); PG8_STAGE(PG8_SB(0, 0), rB2, b2, voffB); PG8_STAGE(PG8_SB(0, 1), rB2, b2 + hstep, voffB); PG8_STAGE(PG8_SA(0, 0), rA2, a2, voffA);
;             PG8_WAIT_V(8); PG8_WAIT_L(0); PG8_BAR; PG8_MMA(1, 0, At, B0); PG8_MMA(1, 1, At, B1); PG8_BAR; PG8_SCHED;
.LBB0_1781:
	v_add_u32_e32 v140, 0x10000, v154
	v_add_u32_e32 v144, 0x14000, v154
	ds_read_b128 v[128:131], v140
	ds_read_b128 v[132:135], v140 offset:1024
	ds_read_b128 v[136:139], v140 offset:2048
	ds_read_b128 v[140:143], v140 offset:3072
	ds_read_b128 v[156:159], v144
	ds_read_b128 v[160:163], v144 offset:1024
	ds_read_b128 v[164:167], v144 offset:2048
	ds_read_b128 v[168:171], v144 offset:3072
	s_add_i32 s6, s61, 0x80
	s_cmp_eq_u32 s45, s63
	s_cselect_b32 s65, s59, s6
	s_cselect_b32 s55, s60, s62
	s_or_b32 s54, s65, 0x80
	s_add_i32 s6, s21, s61
	s_mov_b32 m0, s46
	ds_read_b128 v[172:175], v155
	ds_read_b128 v[176:179], v155 offset:1024
	ds_read_b128 v[180:183], v155 offset:2048
	ds_read_b128 v[184:187], v155 offset:3072
	ds_read_b128 v[194:197], v155 offset:4096
	ds_read_b128 v[198:201], v155 offset:5120
	ds_read_b128 v[202:205], v155 offset:6144
	ds_read_b128 v[206:209], v155 offset:7168
	buffer_load_dwordx4 v148, s[36:39], s6 offen lds
	s_mov_b32 m0, s47
	s_nop 0
	buffer_load_dwordx4 v150, s[36:39], s6 offen lds
	s_waitcnt vmcnt(8)
	s_waitcnt lgkmcnt(0)
	s_barrier
	s_setprio 1
	s_waitcnt lgkmcnt(6)
	v_mfma_f32_16x16x128_f8f6f4 v[120:123], v[128:135], v[172:179], v[120:123]
	v_mfma_f32_16x16x128_f8f6f4 v[124:127], v[136:143], v[172:179], v[124:127]
	s_waitcnt lgkmcnt(4)
	v_mfma_f32_16x16x128_f8f6f4 v[104:107], v[128:135], v[180:187], v[104:107]
	v_mfma_f32_16x16x128_f8f6f4 v[108:111], v[136:143], v[180:187], v[108:111]
	s_waitcnt lgkmcnt(2)
	v_mfma_f32_16x16x128_f8f6f4 v[144:147], v[128:135], v[194:201], v[88:91]
	v_mfma_f32_16x16x128_f8f6f4 v[188:191], v[136:143], v[194:201], v[92:95]
	s_waitcnt lgkmcnt(0)
	v_mfma_f32_16x16x128_f8f6f4 v[210:213], v[128:135], v[202:209], v[72:75]
	v_mfma_f32_16x16x128_f8f6f4 v[214:217], v[136:143], v[202:209], v[76:79]
	s_setprio 0
	s_setprio 1
	v_mfma_f32_16x16x128_f8f6f4 v[112:115], v[156:163], v[172:179], v[112:115]
	v_mfma_f32_16x16x128_f8f6f4 v[116:119], v[164:171], v[172:179], v[116:119]
	v_mfma_f32_16x16x128_f8f6f4 v[96:99], v[156:163], v[180:187], v[96:99]
	v_mfma_f32_16x16x128_f8f6f4 v[100:103], v[164:171], v[180:187], v[100:103]
	v_mfma_f32_16x16x128_f8f6f4 v[172:175], v[156:163], v[194:201], v[80:83]
	v_mfma_f32_16x16x128_f8f6f4 v[176:179], v[164:171], v[194:201], v[84:87]
	v_mfma_f32_16x16x128_f8f6f4 v[180:183], v[156:163], v[202:209], v[64:67]
	v_mfma_f32_16x16x128_f8f6f4 v[184:187], v[164:171], v[202:209], v[68:71]
	s_setprio 0
	s_barrier
	s_mov_b32 m0, s23
	s_mov_b32 s6, s38
	s_mov_b32 s7, s39
	s_nop 0
	ds_read_b128 v[64:67], v155 offset:16384
	ds_read_b128 v[68:71], v155 offset:17408
	ds_read_b128 v[72:75], v155 offset:18432
	ds_read_b128 v[76:79], v155 offset:19456
	ds_read_b128 v[80:83], v155 offset:20480
	ds_read_b128 v[84:87], v155 offset:21504
	ds_read_b128 v[88:91], v155 offset:22528
	ds_read_b128 v[92:95], v155 offset:23552
	buffer_load_dwordx4 v149, s[4:7], s55 offen lds
	s_mov_b32 m0, s24
	s_add_i32 s66, s55, s21
	buffer_load_dwordx4 v151, s[4:7], s55 offen lds
	s_mov_b32 m0, s25
	s_nop 0
	buffer_load_dwordx4 v149, s[4:7], s66 offen lds
	s_mov_b32 m0, s26
	s_nop 0
	buffer_load_dwordx4 v151, s[4:7], s66 offen lds
	s_mov_b32 m0, s22
	s_nop 0
	buffer_load_dwordx4 v148, s[36:39], s65 offen lds
	s_mov_b32 m0, s27
	s_nop 0
	buffer_load_dwordx4 v150, s[36:39], s65 offen lds
	s_waitcnt vmcnt(8)
	s_waitcnt lgkmcnt(0)
	s_barrier
	s_setprio 1
	s_waitcnt lgkmcnt(6)
	v_mfma_f32_16x16x128_f8f6f4 v[56:59], v[128:135], v[64:71], v[56:59]
	v_mfma_f32_16x16x128_f8f6f4 v[60:63], v[136:143], v[64:71], v[60:63]
	s_waitcnt lgkmcnt(0)
	v_mfma_f32_16x16x128_f8f6f4 v[8:11], v[128:135], v[88:95], v[8:11]
	v_mfma_f32_16x16x128_f8f6f4 v[192:195], v[128:135], v[72:79], v[40:43]
	v_mfma_f32_16x16x128_f8f6f4 v[196:199], v[136:143], v[72:79], v[44:47]
	v_mfma_f32_16x16x128_f8f6f4 v[200:203], v[128:135], v[80:87], v[24:27]
	v_mfma_f32_16x16x128_f8f6f4 v[204:207], v[136:143], v[80:87], v[28:31]
	v_mfma_f32_16x16x128_f8f6f4 v[218:221], v[136:143], v[88:95], v[12:15]
	s_setprio 0
	s_setprio 1
	v_mfma_f32_16x16x128_f8f6f4 v[52:55], v[164:171], v[64:71], v[52:55]
	v_mfma_f32_16x16x128_f8f6f4 v[226:229], v[156:163], v[64:71], v[48:51]
	v_mfma_f32_16x16x128_f8f6f4 v[230:233], v[156:163], v[72:79], v[32:35]
	v_mfma_f32_16x16x128_f8f6f4 v[234:237], v[164:171], v[72:79], v[36:39]
	v_mfma_f32_16x16x128_f8f6f4 v[238:241], v[156:163], v[80:87], v[16:19]
	v_mfma_f32_16x16x128_f8f6f4 v[242:245], v[164:171], v[80:87], v[20:23]
	v_mfma_f32_16x16x128_f8f6f4 v[246:249], v[156:163], v[88:95], v[4:7]
	v_mfma_f32_16x16x128_f8f6f4 v[250:253], v[164:171], v[88:95], v[0:3]
	s_setprio 0
	s_barrier
; #define PG8_STAGE(bufoff, rs_, soff_, voff) do { _Pragma("unroll") for (int _i = 0; _i < 2; ++_i) \
;         __builtin_amdgcn_raw_ptr_buffer_load_lds(rs_, (LAS void*)(lds + (bufoff) + ldsw + _i * 8192), 16, (int)(voff)[_i], (int)(soff_), 0, 0); } while (0)
; #define PG8_LDA(dst, b, h) do { _Pragma("unroll") for (int m = 0; m < 4; ++m) dst[m] = PG8_LD2(lds + PG8_SA(b, h) + aoff + m * 2048); } while (0)
; #define PG8_LDB(dst, b, h) do { _Pragma("unroll") for (int n = 0; n < 2; ++n) dst[n] = PG8_LD2(lds + PG8_SB(b, h) + boff + n * 2048); } while (0)
; #define PG8_WAIT_V(n) asm volatile("s_waitcnt vmcnt(" #n ")" ::: "memory")
; #define PG8_WAIT_L(n) asm volatile("s_waitcnt lgkmcnt(" #n ")" ::: "memory")
; #define PG8_BAR __builtin_amdgcn_s_barrier()
; #define PG8_SCHED __builtin_amdgcn_sched_barrier(0)
; template <class Epi, class Sched, bool ALIGN_EPI = false, bool SP2 = false, bool FP8 = false>
; __device__ __forceinline__ void gemm_phase(LAS unsigned char* lds, const Gemm g, const Sched& S, const Epi& E, int wbase) {
;     ...
;             PG8_LDB(B0, 1, 0); PG8_LDB(B1, 1, 1); PG8_SCHED; PG8_LDA(At, 1, 0); PG8_STAGE(PG8_SA(0, 1), rA2, a2 + hstep, voffA);
;             PG8_WAIT_V(8); PG8_WAIT_L(0); PG8_BAR; PG8_MMA(0, 0, At, B0); PG8_MMA(0, 1, At, B1); PG8_BAR; PG8_SCHED;
;             PG8_LDA(At, 1, 1); PG8_STAGE(PG8_SB(1, 0), rB2, b3, voffB); PG8_STAGE(PG8_SB(1, 1), rB2, b3 + hstep, voffB); PG8_STAGE(PG8_SA(1, 0), rA2, a3, voffA);
;             PG8_WAIT_V(8); PG8_WAIT_L(0); PG8_BAR; PG8_MMA(1, 0, At, B0); PG8_MMA(1, 1, At, B1); PG8_BAR; PG8_SCHED;
	s_nop 1
	v_add_u32_e32 v16, 0x18000, v154
	v_add_u32_e32 v20, 0x1c000, v154
	s_nop 0
	ds_read_b128 v[0:3], v16
	ds_read_b128 v[4:7], v16 offset:1024
	ds_read_b128 v[12:15], v16 offset:2048
	ds_read_b128 v[16:19], v16 offset:3072
	ds_read_b128 v[128:131], v20
	ds_read_b128 v[132:135], v20 offset:1024
	ds_read_b128 v[136:139], v20 offset:2048
	ds_read_b128 v[140:143], v20 offset:3072
	s_add_i32 s65, s65, s21
	s_mov_b32 m0, s28
	ds_read_b128 v[20:23], v155 offset:32768
	ds_read_b128 v[24:27], v155 offset:33792
	ds_read_b128 v[28:31], v155 offset:34816
	ds_read_b128 v[32:35], v155 offset:35840
	ds_read_b128 v[36:39], v155 offset:36864
	ds_read_b128 v[40:43], v155 offset:37888
	ds_read_b128 v[44:47], v155 offset:38912
	ds_read_b128 v[48:51], v155 offset:39936
	buffer_load_dwordx4 v148, s[36:39], s65 offen lds
	s_mov_b32 m0, s29
	s_nop 0
	buffer_load_dwordx4 v150, s[36:39], s65 offen lds
	s_waitcnt vmcnt(8)
	s_waitcnt lgkmcnt(0)
	s_barrier
	s_setprio 1
	s_waitcnt lgkmcnt(6)
	v_mfma_f32_16x16x128_f8f6f4 v[120:123], v[0:7], v[20:27], v[120:123]
	v_mfma_f32_16x16x128_f8f6f4 v[124:127], v[12:19], v[20:27], v[124:127]
	s_waitcnt lgkmcnt(4)
	v_mfma_f32_16x16x128_f8f6f4 v[104:107], v[0:7], v[28:35], v[104:107]
	v_mfma_f32_16x16x128_f8f6f4 v[108:111], v[12:19], v[28:35], v[108:111]
	s_waitcnt lgkmcnt(2)
	v_mfma_f32_16x16x128_f8f6f4 v[88:91], v[0:7], v[36:43], v[144:147]
	v_mfma_f32_16x16x128_f8f6f4 v[92:95], v[12:19], v[36:43], v[188:191]
	s_waitcnt lgkmcnt(0)
	v_mfma_f32_16x16x128_f8f6f4 v[72:75], v[0:7], v[44:51], v[210:213]
	v_mfma_f32_16x16x128_f8f6f4 v[76:79], v[12:19], v[44:51], v[214:217]
	s_setprio 0
	s_setprio 1
	v_mfma_f32_16x16x128_f8f6f4 v[112:115], v[128:135], v[20:27], v[112:115]
	v_mfma_f32_16x16x128_f8f6f4 v[116:119], v[136:143], v[20:27], v[116:119]
	v_mfma_f32_16x16x128_f8f6f4 v[96:99], v[128:135], v[28:35], v[96:99]
	v_mfma_f32_16x16x128_f8f6f4 v[100:103], v[136:143], v[28:35], v[100:103]
	v_mfma_f32_16x16x128_f8f6f4 v[80:83], v[128:135], v[36:43], v[172:175]
	v_mfma_f32_16x16x128_f8f6f4 v[84:87], v[136:143], v[36:43], v[176:179]
	v_mfma_f32_16x16x128_f8f6f4 v[64:67], v[128:135], v[44:51], v[180:183]
	v_mfma_f32_16x16x128_f8f6f4 v[68:71], v[136:143], v[44:51], v[184:187]
	s_setprio 0
	s_barrier
	s_mov_b32 m0, s30
	s_bitset1_b32 s55, 7
	ds_read_b128 v[32:35], v155 offset:49152
	ds_read_b128 v[36:39], v155 offset:50176
	ds_read_b128 v[156:159], v155 offset:51200
	ds_read_b128 v[160:163], v155 offset:52224
	ds_read_b128 v[164:167], v155 offset:53248
	ds_read_b128 v[168:171], v155 offset:54272
	ds_read_b128 v[172:175], v155 offset:55296
	ds_read_b128 v[176:179], v155 offset:56320
	buffer_load_dwordx4 v149, s[4:7], s55 offen lds
	s_mov_b32 m0, s31
	s_nop 0
	buffer_load_dwordx4 v151, s[4:7], s55 offen lds
	s_add_i32 s55, s55, s21
	s_mov_b32 m0, s35
	s_nop 0
	buffer_load_dwordx4 v149, s[4:7], s55 offen lds
	s_mov_b32 m0, s41
	s_nop 0
	buffer_load_dwordx4 v151, s[4:7], s55 offen lds
	s_mov_b32 m0, s33
	s_nop 0
	buffer_load_dwordx4 v148, s[36:39], s54 offen lds
	s_mov_b32 m0, s34
	s_nop 0
	buffer_load_dwordx4 v150, s[36:39], s54 offen lds
	s_waitcnt vmcnt(8)
	s_waitcnt lgkmcnt(0)
	s_barrier
	s_setprio 1
	s_waitcnt lgkmcnt(6)
	v_mfma_f32_16x16x128_f8f6f4 v[56:59], v[0:7], v[32:39], v[56:59]
	v_mfma_f32_16x16x128_f8f6f4 v[60:63], v[12:19], v[32:39], v[60:63]
	s_waitcnt lgkmcnt(4)
	v_mfma_f32_16x16x128_f8f6f4 v[40:43], v[0:7], v[156:163], v[192:195]
	v_mfma_f32_16x16x128_f8f6f4 v[44:47], v[12:19], v[156:163], v[196:199]
	s_waitcnt lgkmcnt(2)
	v_mfma_f32_16x16x128_f8f6f4 v[24:27], v[0:7], v[164:171], v[200:203]
	v_mfma_f32_16x16x128_f8f6f4 v[28:31], v[12:19], v[164:171], v[204:207]
	s_waitcnt lgkmcnt(0)
	v_mfma_f32_16x16x128_f8f6f4 v[8:11], v[0:7], v[172:179], v[8:11]
	v_mfma_f32_16x16x128_f8f6f4 v[12:15], v[12:19], v[172:179], v[218:221]
	s_setprio 0
	s_setprio 1
	v_mfma_f32_16x16x128_f8f6f4 v[48:51], v[128:135], v[32:39], v[226:229]
	v_mfma_f32_16x16x128_f8f6f4 v[52:55], v[136:143], v[32:39], v[52:55]
	v_mfma_f32_16x16x128_f8f6f4 v[32:35], v[128:135], v[156:163], v[230:233]
	v_mfma_f32_16x16x128_f8f6f4 v[36:39], v[136:143], v[156:163], v[234:237]
	v_mfma_f32_16x16x128_f8f6f4 v[16:19], v[128:135], v[164:171], v[238:241]
	v_mfma_f32_16x16x128_f8f6f4 v[20:23], v[136:143], v[164:171], v[242:245]
	v_mfma_f32_16x16x128_f8f6f4 v[4:7], v[128:135], v[172:179], v[246:249]
	v_mfma_f32_16x16x128_f8f6f4 v[0:3], v[136:143], v[172:179], v[250:253]
	s_setprio 0
	s_barrier
	s_add_i32 s63, s63, 2
	s_addk_i32 s61, 0x100
	s_addk_i32 s62, 0x100
	s_cmp_ge_i32 s63, s43
	s_cbranch_scc0 .LBB0_1781
	v_mov_b32_e32 v230, v222
	v_mov_b32_e32 v233, v223
	v_mov_b32_e32 v231, v225
	v_mov_b32_e32 v234, 0xff61b1e6
	s_and_b64 vcc, exec, s[16:17]
	s_cbranch_vccnz .LBB0_1784
	s_branch .LBB0_1785

; #define PG8_STAGE(bufoff, rs_, soff_, voff) do { _Pragma("unroll") for (int _i = 0; _i < 2; ++_i) \
;         __builtin_amdgcn_raw_ptr_buffer_load_lds(rs_, (LAS void*)(lds + (bufoff) + ldsw + _i * 8192), 16, (int)(voff)[_i], (int)(soff_), 0, 0); } while (0)
; #define PG8_LDA(dst, b, h) do { _Pragma("unroll") for (int m = 0; m < 4; ++m) dst[m] = PG8_LD2(lds + PG8_SA(b, h) + aoff + m * 2048); } while (0)
; #define PG8_LDB(dst, b, h) do { _Pragma("unroll") for (int n = 0; n < 2; ++n) dst[n] = PG8_LD2(lds + PG8_SB(b, h) + boff + n * 2048); } while (0)
; #define PG8_WAIT_V(n) asm volatile("s_waitcnt vmcnt(" #n ")" ::: "memory")
; #define PG8_WAIT_L(n) asm volatile("s_waitcnt lgkmcnt(" #n ")" ::: "memory")
; #define PG8_BAR __builtin_amdgcn_s_barrier()
; #define PG8_SCHED __builtin_amdgcn_sched_barrier(0)
; template <class Epi, class Sched, bool ALIGN_EPI = false, bool SP2 = false, bool FP8 = false>
; __device__ __forceinline__ void gemm_phase(LAS unsigned char* lds, const Gemm g, const Sched& S, const Epi& E, int wbase) {
;     ...
;             PG8_LDB(B0, 0, 0); PG8_LDB(B1, 0, 1); PG8_SCHED; PG8_LDA(At, 0, 0); PG8_STAGE(PG8_SA(1, 1), rAc, a1 + hstep, voffA);
;             PG8_WAIT_V(8); PG8_WAIT_L(0); PG8_BAR; PG8_MMA(0, 0, At, B0); PG8_MMA(0, 1, At, B1); PG8_BAR; PG8_SCHED;
;             PG8_LDA(At, 0, 1); PG8_STAGE(PG8_SB(0, 0), rB2, b2, voffB); PG8_STAGE(PG8_SB(0, 1), rB2, b2 + hstep, voffB); PG8_STAGE(PG8_SA(0, 0), rA2, a2, voffA);
;             PG8_WAIT_V(8); PG8_WAIT_L(0); PG8_BAR; PG8_MMA(1, 0, At, B0); PG8_MMA(1, 1, At, B1); PG8_BAR; PG8_SCHED;
.LBB0_1854:
	v_add_u32_e32 v140, 0x10000, v176
	v_add_u32_e32 v156, 0x14000, v176
	ds_read_b128 v[128:131], v140
	ds_read_b128 v[132:135], v140 offset:1024
	ds_read_b128 v[136:139], v140 offset:2048
	ds_read_b128 v[140:143], v140 offset:3072
	ds_read_b128 v[144:147], v156
	ds_read_b128 v[148:151], v156 offset:1024
	ds_read_b128 v[152:155], v156 offset:2048
	ds_read_b128 v[156:159], v156 offset:3072
	s_add_i32 s6, s65, 0x80
	s_cmp_eq_u32 s52, s67
	s_cselect_b32 s68, s21, s6
	s_cselect_b32 s55, s63, s66
	s_or_b32 s54, s68, 0x80
	s_add_i32 s6, s24, s65
	s_mov_b32 m0, s53
	ds_read_b128 v[160:163], v177
	ds_read_b128 v[164:167], v177 offset:1024
	ds_read_b128 v[178:181], v177 offset:2048
	ds_read_b128 v[182:185], v177 offset:3072
	ds_read_b128 v[194:197], v177 offset:4096
	ds_read_b128 v[198:201], v177 offset:5120
	ds_read_b128 v[202:205], v177 offset:6144
	ds_read_b128 v[206:209], v177 offset:7168
	buffer_load_dwordx4 v170, s[36:39], s6 offen lds
	s_mov_b32 m0, s56
	s_nop 0
	buffer_load_dwordx4 v172, s[36:39], s6 offen lds
	s_waitcnt vmcnt(8)
	s_waitcnt lgkmcnt(0)
	s_barrier
	s_setprio 1
	s_waitcnt lgkmcnt(6)
	v_mfma_f32_16x16x128_f8f6f4 v[124:127], v[128:135], v[160:167], v[124:127]
	v_mfma_f32_16x16x128_f8f6f4 v[120:123], v[136:143], v[160:167], v[120:123]
	s_waitcnt lgkmcnt(4)
	v_mfma_f32_16x16x128_f8f6f4 v[108:111], v[128:135], v[178:185], v[108:111]
	v_mfma_f32_16x16x128_f8f6f4 v[104:107], v[136:143], v[178:185], v[104:107]
	s_waitcnt lgkmcnt(2)
	v_mfma_f32_16x16x128_f8f6f4 v[186:189], v[128:135], v[194:201], v[92:95]
	v_mfma_f32_16x16x128_f8f6f4 v[190:193], v[136:143], v[194:201], v[88:91]
	s_waitcnt lgkmcnt(0)
	v_mfma_f32_16x16x128_f8f6f4 v[210:213], v[128:135], v[202:209], v[76:79]
	v_mfma_f32_16x16x128_f8f6f4 v[214:217], v[136:143], v[202:209], v[72:75]
	s_setprio 0
	s_setprio 1
	v_mfma_f32_16x16x128_f8f6f4 v[116:119], v[144:151], v[160:167], v[116:119]
	v_mfma_f32_16x16x128_f8f6f4 v[112:115], v[152:159], v[160:167], v[112:115]
	v_mfma_f32_16x16x128_f8f6f4 v[100:103], v[144:151], v[178:185], v[100:103]
	v_mfma_f32_16x16x128_f8f6f4 v[96:99], v[152:159], v[178:185], v[96:99]
	v_mfma_f32_16x16x128_f8f6f4 v[160:163], v[144:151], v[194:201], v[84:87]
	v_mfma_f32_16x16x128_f8f6f4 v[164:167], v[152:159], v[194:201], v[80:83]
	v_mfma_f32_16x16x128_f8f6f4 v[178:181], v[144:151], v[202:209], v[68:71]
	v_mfma_f32_16x16x128_f8f6f4 v[182:185], v[152:159], v[202:209], v[64:67]
	s_setprio 0
	s_barrier
	s_mov_b32 m0, s26
	s_mov_b32 s6, s38
	s_mov_b32 s7, s39
	s_nop 1
	ds_read_b128 v[64:67], v177 offset:16384
	ds_read_b128 v[68:71], v177 offset:17408
	ds_read_b128 v[72:75], v177 offset:18432
	ds_read_b128 v[76:79], v177 offset:19456
	ds_read_b128 v[80:83], v177 offset:20480
	ds_read_b128 v[84:87], v177 offset:21504
	ds_read_b128 v[88:91], v177 offset:22528
	ds_read_b128 v[92:95], v177 offset:23552
	buffer_load_dwordx4 v171, s[4:7], s55 offen lds
	s_mov_b32 m0, s27
	s_add_i32 s69, s55, s24
	buffer_load_dwordx4 v173, s[4:7], s55 offen lds
	s_mov_b32 m0, s28
	s_nop 0
	buffer_load_dwordx4 v171, s[4:7], s69 offen lds
	s_mov_b32 m0, s29
	s_nop 0
	buffer_load_dwordx4 v173, s[4:7], s69 offen lds
	s_mov_b32 m0, s25
	s_nop 0
	buffer_load_dwordx4 v170, s[36:39], s68 offen lds
	s_mov_b32 m0, s30
	s_nop 0
	buffer_load_dwordx4 v172, s[36:39], s68 offen lds
	s_waitcnt vmcnt(8)
	s_waitcnt lgkmcnt(0)
	s_barrier
	s_setprio 1
	s_waitcnt lgkmcnt(6)
	v_mfma_f32_16x16x128_f8f6f4 v[60:63], v[128:135], v[64:71], v[60:63]
	v_mfma_f32_16x16x128_f8f6f4 v[56:59], v[136:143], v[64:71], v[56:59]
	s_waitcnt lgkmcnt(4)
	v_mfma_f32_16x16x128_f8f6f4 v[194:197], v[128:135], v[72:79], v[44:47]
	v_mfma_f32_16x16x128_f8f6f4 v[198:201], v[136:143], v[72:79], v[40:43]
	s_waitcnt lgkmcnt(2)
	v_mfma_f32_16x16x128_f8f6f4 v[202:205], v[128:135], v[80:87], v[28:31]
	v_mfma_f32_16x16x128_f8f6f4 v[206:209], v[136:143], v[80:87], v[24:27]
	s_waitcnt lgkmcnt(0)
	v_mfma_f32_16x16x128_f8f6f4 v[218:221], v[128:135], v[88:95], v[12:15]
	v_mfma_f32_16x16x128_f8f6f4 v[226:229], v[136:143], v[88:95], v[8:11]
	s_setprio 0
	s_setprio 1
	v_mfma_f32_16x16x128_f8f6f4 v[52:55], v[144:151], v[64:71], v[52:55]
	v_mfma_f32_16x16x128_f8f6f4 v[48:51], v[152:159], v[64:71], v[48:51]
	v_mfma_f32_16x16x128_f8f6f4 v[230:233], v[144:151], v[72:79], v[36:39]
	v_mfma_f32_16x16x128_f8f6f4 v[234:237], v[152:159], v[72:79], v[32:35]
	v_mfma_f32_16x16x128_f8f6f4 v[238:241], v[144:151], v[80:87], v[20:23]
	v_mfma_f32_16x16x128_f8f6f4 v[242:245], v[152:159], v[80:87], v[16:19]
	v_mfma_f32_16x16x128_f8f6f4 v[246:249], v[144:151], v[88:95], v[4:7]
	v_mfma_f32_16x16x128_f8f6f4 v[250:253], v[152:159], v[88:95], v[0:3]
	s_setprio 0
	s_barrier
; #define PG8_STAGE(bufoff, rs_, soff_, voff) do { _Pragma("unroll") for (int _i = 0; _i < 2; ++_i) \
;         __builtin_amdgcn_raw_ptr_buffer_load_lds(rs_, (LAS void*)(lds + (bufoff) + ldsw + _i * 8192), 16, (int)(voff)[_i], (int)(soff_), 0, 0); } while (0)
; #define PG8_LDA(dst, b, h) do { _Pragma("unroll") for (int m = 0; m < 4; ++m) dst[m] = PG8_LD2(lds + PG8_SA(b, h) + aoff + m * 2048); } while (0)
; #define PG8_LDB(dst, b, h) do { _Pragma("unroll") for (int n = 0; n < 2; ++n) dst[n] = PG8_LD2(lds + PG8_SB(b, h) + boff + n * 2048); } while (0)
; #define PG8_WAIT_V(n) asm volatile("s_waitcnt vmcnt(" #n ")" ::: "memory")
; #define PG8_WAIT_L(n) asm volatile("s_waitcnt lgkmcnt(" #n ")" ::: "memory")
; #define PG8_BAR __builtin_amdgcn_s_barrier()
; #define PG8_SCHED __builtin_amdgcn_sched_barrier(0)
; template <class Epi, class Sched, bool ALIGN_EPI = false, bool SP2 = false, bool FP8 = false>
; __device__ __forceinline__ void gemm_phase(LAS unsigned char* lds, const Gemm g, const Sched& S, const Epi& E, int wbase) {
;     ...
;             PG8_LDB(B0, 1, 0); PG8_LDB(B1, 1, 1); PG8_SCHED; PG8_LDA(At, 1, 0); PG8_STAGE(PG8_SA(0, 1), rA2, a2 + hstep, voffA);
;             PG8_WAIT_V(8); PG8_WAIT_L(0); PG8_BAR; PG8_MMA(0, 0, At, B0); PG8_MMA(0, 1, At, B1); PG8_BAR; PG8_SCHED;
;             PG8_LDA(At, 1, 1); PG8_STAGE(PG8_SB(1, 0), rB2, b3, voffB); PG8_STAGE(PG8_SB(1, 1), rB2, b3 + hstep, voffB); PG8_STAGE(PG8_SA(1, 0), rA2, a3, voffA);
;             PG8_WAIT_V(8); PG8_WAIT_L(0); PG8_BAR; PG8_MMA(1, 0, At, B0); PG8_MMA(1, 1, At, B1); PG8_BAR; PG8_SCHED;
	v_add_u32_e32 v8, 0x18000, v176
	s_nop 3
	ds_read_b128 v[0:3], v8
	ds_read_b128 v[4:7], v8 offset:1024
	ds_read_b128 v[16:19], v8 offset:2048
	ds_read_b128 v[20:23], v8 offset:3072
	v_add_u32_e32 v8, 0x1c000, v176
	ds_read_b128 v[128:131], v8
	ds_read_b128 v[132:135], v8 offset:1024
	ds_read_b128 v[136:139], v8 offset:2048
	ds_read_b128 v[140:143], v8 offset:3072
	s_add_i32 s68, s68, s24
	s_mov_b32 m0, s31
	ds_read_b128 v[8:11], v177 offset:32768
	ds_read_b128 v[12:15], v177 offset:33792
	ds_read_b128 v[24:27], v177 offset:34816
	ds_read_b128 v[28:31], v177 offset:35840
	ds_read_b128 v[32:35], v177 offset:36864
	ds_read_b128 v[36:39], v177 offset:37888
	ds_read_b128 v[40:43], v177 offset:38912
	ds_read_b128 v[44:47], v177 offset:39936
	buffer_load_dwordx4 v170, s[36:39], s68 offen lds
	s_mov_b32 m0, s33
	s_nop 0
	buffer_load_dwordx4 v172, s[36:39], s68 offen lds
	s_waitcnt vmcnt(8)
	s_waitcnt lgkmcnt(0)
	s_barrier
	s_setprio 1
	s_waitcnt lgkmcnt(6)
	v_mfma_f32_16x16x128_f8f6f4 v[124:127], v[0:7], v[8:15], v[124:127]
	v_mfma_f32_16x16x128_f8f6f4 v[120:123], v[16:23], v[8:15], v[120:123]
	s_waitcnt lgkmcnt(4)
	v_mfma_f32_16x16x128_f8f6f4 v[108:111], v[0:7], v[24:31], v[108:111]
	v_mfma_f32_16x16x128_f8f6f4 v[104:107], v[16:23], v[24:31], v[104:107]
	s_waitcnt lgkmcnt(2)
	v_mfma_f32_16x16x128_f8f6f4 v[92:95], v[0:7], v[32:39], v[186:189]
	v_mfma_f32_16x16x128_f8f6f4 v[88:91], v[16:23], v[32:39], v[190:193]
	s_waitcnt lgkmcnt(0)
	v_mfma_f32_16x16x128_f8f6f4 v[76:79], v[0:7], v[40:47], v[210:213]
	v_mfma_f32_16x16x128_f8f6f4 v[72:75], v[16:23], v[40:47], v[214:217]
	s_setprio 0
	s_setprio 1
	v_mfma_f32_16x16x128_f8f6f4 v[116:119], v[128:135], v[8:15], v[116:119]
	v_mfma_f32_16x16x128_f8f6f4 v[112:115], v[136:143], v[8:15], v[112:115]
	v_mfma_f32_16x16x128_f8f6f4 v[100:103], v[128:135], v[24:31], v[100:103]
	v_mfma_f32_16x16x128_f8f6f4 v[96:99], v[136:143], v[24:31], v[96:99]
	v_mfma_f32_16x16x128_f8f6f4 v[84:87], v[128:135], v[32:39], v[160:163]
	v_mfma_f32_16x16x128_f8f6f4 v[80:83], v[136:143], v[32:39], v[164:167]
	v_mfma_f32_16x16x128_f8f6f4 v[68:71], v[128:135], v[40:47], v[178:181]
	v_mfma_f32_16x16x128_f8f6f4 v[64:67], v[136:143], v[40:47], v[182:185]
	s_setprio 0
	s_barrier
	s_mov_b32 m0, s34
	s_bitset1_b32 s55, 7
	ds_read_b128 v[32:35], v177 offset:49152
	ds_read_b128 v[36:39], v177 offset:50176
	ds_read_b128 v[144:147], v177 offset:51200
	ds_read_b128 v[148:151], v177 offset:52224
	ds_read_b128 v[152:155], v177 offset:53248
	ds_read_b128 v[156:159], v177 offset:54272
	ds_read_b128 v[160:163], v177 offset:55296
	ds_read_b128 v[164:167], v177 offset:56320
	buffer_load_dwordx4 v171, s[4:7], s55 offen lds
	s_mov_b32 m0, s35
	s_nop 0
	buffer_load_dwordx4 v173, s[4:7], s55 offen lds
	s_add_i32 s55, s55, s24
	s_mov_b32 m0, s43
	s_nop 0
	buffer_load_dwordx4 v171, s[4:7], s55 offen lds
	s_mov_b32 m0, s44
	s_nop 0
	buffer_load_dwordx4 v173, s[4:7], s55 offen lds
	s_mov_b32 m0, s41
	s_nop 0
	buffer_load_dwordx4 v170, s[36:39], s54 offen lds
	s_mov_b32 m0, s42
	s_nop 0
	buffer_load_dwordx4 v172, s[36:39], s54 offen lds
	s_waitcnt vmcnt(8)
	s_waitcnt lgkmcnt(0)
	s_barrier
	s_setprio 1
	s_waitcnt lgkmcnt(6)
	v_mfma_f32_16x16x128_f8f6f4 v[60:63], v[0:7], v[32:39], v[60:63]
	v_mfma_f32_16x16x128_f8f6f4 v[56:59], v[16:23], v[32:39], v[56:59]
	s_waitcnt lgkmcnt(4)
	v_mfma_f32_16x16x128_f8f6f4 v[44:47], v[0:7], v[144:151], v[194:197]
	v_mfma_f32_16x16x128_f8f6f4 v[40:43], v[16:23], v[144:151], v[198:201]
	s_waitcnt lgkmcnt(2)
	v_mfma_f32_16x16x128_f8f6f4 v[28:31], v[0:7], v[152:159], v[202:205]
	v_mfma_f32_16x16x128_f8f6f4 v[24:27], v[16:23], v[152:159], v[206:209]
	s_waitcnt lgkmcnt(0)
	v_mfma_f32_16x16x128_f8f6f4 v[12:15], v[0:7], v[160:167], v[218:221]
	v_mfma_f32_16x16x128_f8f6f4 v[8:11], v[16:23], v[160:167], v[226:229]
	s_setprio 0
	s_setprio 1
	v_mfma_f32_16x16x128_f8f6f4 v[52:55], v[128:135], v[32:39], v[52:55]
	v_mfma_f32_16x16x128_f8f6f4 v[48:51], v[136:143], v[32:39], v[48:51]
	v_mfma_f32_16x16x128_f8f6f4 v[36:39], v[128:135], v[144:151], v[230:233]
	v_mfma_f32_16x16x128_f8f6f4 v[32:35], v[136:143], v[144:151], v[234:237]
	v_mfma_f32_16x16x128_f8f6f4 v[20:23], v[128:135], v[152:159], v[238:241]
	v_mfma_f32_16x16x128_f8f6f4 v[16:19], v[136:143], v[152:159], v[242:245]
	v_mfma_f32_16x16x128_f8f6f4 v[4:7], v[128:135], v[160:167], v[246:249]
	v_mfma_f32_16x16x128_f8f6f4 v[0:3], v[136:143], v[160:167], v[250:253]
	s_setprio 0
	s_barrier
	s_add_i32 s67, s67, 2
	s_addk_i32 s65, 0x100
	s_addk_i32 s66, 0x100
	s_cmp_ge_i32 s67, s47
	s_cbranch_scc0 .LBB0_1854
	v_readlane_b32 s68, v255, 22
	v_readlane_b32 s69, v255, 23
	v_mov_b32_e32 v230, v168
	v_mov_b32_e32 v233, v169
	v_mov_b32_e32 v231, v222
	v_mov_b32_e32 v234, v223
	s_and_b64 vcc, exec, s[16:17]
	s_cbranch_vccnz .LBB0_1857
	s_branch .LBB0_1858

; #define PG8_STAGE(bufoff, rs_, soff_, voff) do { _Pragma("unroll") for (int _i = 0; _i < 2; ++_i) \
;         __builtin_amdgcn_raw_ptr_buffer_load_lds(rs_, (LAS void*)(lds + (bufoff) + ldsw + _i * 8192), 16, (int)(voff)[_i], (int)(soff_), 0, 0); } while (0)
; #define PG8_LDA(dst, b, h) do { _Pragma("unroll") for (int m = 0; m < 4; ++m) dst[m] = PG8_LD2(lds + PG8_SA(b, h) + aoff + m * 2048); } while (0)
; #define PG8_LDB(dst, b, h) do { _Pragma("unroll") for (int n = 0; n < 2; ++n) dst[n] = PG8_LD2(lds + PG8_SB(b, h) + boff + n * 2048); } while (0)
; #define PG8_WAIT_V(n) asm volatile("s_waitcnt vmcnt(" #n ")" ::: "memory")
; #define PG8_WAIT_L(n) asm volatile("s_waitcnt lgkmcnt(" #n ")" ::: "memory")
; #define PG8_BAR __builtin_amdgcn_s_barrier()
; #define PG8_SCHED __builtin_amdgcn_sched_barrier(0)
; template <class Epi, class Sched, bool ALIGN_EPI = false, bool SP2 = false, bool FP8 = false>
; __device__ __forceinline__ void gemm_phase(LAS unsigned char* lds, const Gemm g, const Sched& S, const Epi& E, int wbase) {
;     ...
;             PG8_LDB(B0, 0, 0); PG8_LDB(B1, 0, 1); PG8_SCHED; PG8_LDA(At, 0, 0); PG8_STAGE(PG8_SA(1, 1), rAc, a1 + hstep, voffA);
;             PG8_WAIT_V(8); PG8_WAIT_L(0); PG8_BAR; PG8_MMA(0, 0, At, B0); PG8_MMA(0, 1, At, B1); PG8_BAR; PG8_SCHED;
;             PG8_LDA(At, 0, 1); PG8_STAGE(PG8_SB(0, 0), rB2, b2, voffB); PG8_STAGE(PG8_SB(0, 1), rB2, b2 + hstep, voffB); PG8_STAGE(PG8_SA(0, 0), rA2, a2, voffA);
;             PG8_WAIT_V(8); PG8_WAIT_L(0); PG8_BAR; PG8_MMA(1, 0, At, B0); PG8_MMA(1, 1, At, B1); PG8_BAR; PG8_SCHED;
.LBB0_1990:
	v_add_u32_e32 v136, 0x10000, v180
	v_add_u32_e32 v156, 0x14000, v180
	ds_read_b128 v[120:123], v136
	ds_read_b128 v[124:127], v136 offset:1024
	ds_read_b128 v[132:135], v136 offset:2048
	ds_read_b128 v[136:139], v136 offset:3072
	ds_read_b128 v[144:147], v156
	ds_read_b128 v[148:151], v156 offset:1024
	ds_read_b128 v[152:155], v156 offset:2048
	ds_read_b128 v[156:159], v156 offset:3072
	s_add_i32 s14, s4, 0x80
	s_cmp_eq_u32 s84, s61
	s_cselect_b32 s62, s2, s14
	s_cselect_b32 s55, s3, s5
	s_or_b32 s54, s62, 0x80
	s_add_i32 s14, s42, s4
	s_mov_b32 m0, s85
	ds_read_b128 v[160:163], v181
	ds_read_b128 v[164:167], v181 offset:1024
	ds_read_b128 v[182:185], v181 offset:2048
	ds_read_b128 v[186:189], v181 offset:3072
	ds_read_b128 v[194:197], v181 offset:4096
	ds_read_b128 v[198:201], v181 offset:5120
	ds_read_b128 v[202:205], v181 offset:6144
	ds_read_b128 v[206:209], v181 offset:7168
	buffer_load_dwordx4 v174, s[36:39], s14 offen lds
	s_mov_b32 m0, s8
	s_nop 0
	buffer_load_dwordx4 v176, s[36:39], s14 offen lds
	s_waitcnt vmcnt(8)
	s_waitcnt lgkmcnt(0)
	s_barrier
	s_setprio 1
	s_waitcnt lgkmcnt(6)
	v_mfma_f32_16x16x128_f8f6f4 v[140:143], v[120:127], v[160:167], v[140:143]
	v_mfma_f32_16x16x128_f8f6f4 v[128:131], v[132:139], v[160:167], v[128:131]
	s_waitcnt lgkmcnt(4)
	v_mfma_f32_16x16x128_f8f6f4 v[108:111], v[120:127], v[182:189], v[108:111]
	v_mfma_f32_16x16x128_f8f6f4 v[104:107], v[132:139], v[182:189], v[104:107]
	s_waitcnt lgkmcnt(2)
	v_mfma_f32_16x16x128_f8f6f4 v[168:171], v[120:127], v[194:201], v[92:95]
	v_mfma_f32_16x16x128_f8f6f4 v[190:193], v[132:139], v[194:201], v[88:91]
	s_waitcnt lgkmcnt(0)
	v_mfma_f32_16x16x128_f8f6f4 v[210:213], v[120:127], v[202:209], v[76:79]
	v_mfma_f32_16x16x128_f8f6f4 v[214:217], v[132:139], v[202:209], v[72:75]
	s_setprio 0
	s_setprio 1
	v_mfma_f32_16x16x128_f8f6f4 v[116:119], v[144:151], v[160:167], v[116:119]
	v_mfma_f32_16x16x128_f8f6f4 v[112:115], v[152:159], v[160:167], v[112:115]
	v_mfma_f32_16x16x128_f8f6f4 v[100:103], v[144:151], v[182:189], v[100:103]
	v_mfma_f32_16x16x128_f8f6f4 v[96:99], v[152:159], v[182:189], v[96:99]
	v_mfma_f32_16x16x128_f8f6f4 v[160:163], v[144:151], v[194:201], v[84:87]
	v_mfma_f32_16x16x128_f8f6f4 v[164:167], v[152:159], v[194:201], v[80:83]
	v_mfma_f32_16x16x128_f8f6f4 v[182:185], v[144:151], v[202:209], v[68:71]
	v_mfma_f32_16x16x128_f8f6f4 v[186:189], v[152:159], v[202:209], v[64:67]
	s_setprio 0
	s_barrier
	s_mov_b32 m0, s44
	s_mov_b32 s14, s38
	s_mov_b32 s15, s39
	s_nop 1
	ds_read_b128 v[64:67], v181 offset:16384
	ds_read_b128 v[68:71], v181 offset:17408
	ds_read_b128 v[72:75], v181 offset:18432
	ds_read_b128 v[76:79], v181 offset:19456
	ds_read_b128 v[80:83], v181 offset:20480
	ds_read_b128 v[84:87], v181 offset:21504
	ds_read_b128 v[88:91], v181 offset:22528
	ds_read_b128 v[92:95], v181 offset:23552
	buffer_load_dwordx4 v175, s[12:15], s55 offen lds
	s_mov_b32 m0, s45
	s_add_i32 s63, s55, s42
	buffer_load_dwordx4 v177, s[12:15], s55 offen lds
	s_mov_b32 m0, s46
	s_nop 0
	buffer_load_dwordx4 v175, s[12:15], s63 offen lds
	s_mov_b32 m0, s47
	s_nop 0
	buffer_load_dwordx4 v177, s[12:15], s63 offen lds
	s_mov_b32 m0, s43
	s_nop 0
	buffer_load_dwordx4 v174, s[36:39], s62 offen lds
	s_mov_b32 m0, s48
	s_nop 0
	buffer_load_dwordx4 v176, s[36:39], s62 offen lds
	s_waitcnt vmcnt(8)
	s_waitcnt lgkmcnt(0)
	s_barrier
	s_setprio 1
	s_waitcnt lgkmcnt(6)
	v_mfma_f32_16x16x128_f8f6f4 v[60:63], v[120:127], v[64:71], v[60:63]
	v_mfma_f32_16x16x128_f8f6f4 v[56:59], v[132:139], v[64:71], v[56:59]
	s_waitcnt lgkmcnt(4)
	v_mfma_f32_16x16x128_f8f6f4 v[194:197], v[120:127], v[72:79], v[44:47]
	v_mfma_f32_16x16x128_f8f6f4 v[198:201], v[132:139], v[72:79], v[40:43]
	s_waitcnt lgkmcnt(2)
	v_mfma_f32_16x16x128_f8f6f4 v[202:205], v[120:127], v[80:87], v[28:31]
	v_mfma_f32_16x16x128_f8f6f4 v[206:209], v[132:139], v[80:87], v[24:27]
	s_waitcnt lgkmcnt(0)
	v_mfma_f32_16x16x128_f8f6f4 v[218:221], v[120:127], v[88:95], v[12:15]
	v_mfma_f32_16x16x128_f8f6f4 v[226:229], v[132:139], v[88:95], v[8:11]
	s_setprio 0
	s_setprio 1
	v_mfma_f32_16x16x128_f8f6f4 v[52:55], v[144:151], v[64:71], v[52:55]
	v_mfma_f32_16x16x128_f8f6f4 v[48:51], v[152:159], v[64:71], v[48:51]
	v_mfma_f32_16x16x128_f8f6f4 v[230:233], v[144:151], v[72:79], v[36:39]
	v_mfma_f32_16x16x128_f8f6f4 v[234:237], v[152:159], v[72:79], v[32:35]
	v_mfma_f32_16x16x128_f8f6f4 v[238:241], v[144:151], v[80:87], v[20:23]
	v_mfma_f32_16x16x128_f8f6f4 v[242:245], v[152:159], v[80:87], v[16:19]
	v_mfma_f32_16x16x128_f8f6f4 v[246:249], v[144:151], v[88:95], v[4:7]
	v_mfma_f32_16x16x128_f8f6f4 v[250:253], v[152:159], v[88:95], v[0:3]
	s_setprio 0
	s_barrier
; #define PG8_STAGE(bufoff, rs_, soff_, voff) do { _Pragma("unroll") for (int _i = 0; _i < 2; ++_i) \
;         __builtin_amdgcn_raw_ptr_buffer_load_lds(rs_, (LAS void*)(lds + (bufoff) + ldsw + _i * 8192), 16, (int)(voff)[_i], (int)(soff_), 0, 0); } while (0)
; #define PG8_LDA(dst, b, h) do { _Pragma("unroll") for (int m = 0; m < 4; ++m) dst[m] = PG8_LD2(lds + PG8_SA(b, h) + aoff + m * 2048); } while (0)
; #define PG8_LDB(dst, b, h) do { _Pragma("unroll") for (int n = 0; n < 2; ++n) dst[n] = PG8_LD2(lds + PG8_SB(b, h) + boff + n * 2048); } while (0)
; #define PG8_WAIT_V(n) asm volatile("s_waitcnt vmcnt(" #n ")" ::: "memory")
; #define PG8_WAIT_L(n) asm volatile("s_waitcnt lgkmcnt(" #n ")" ::: "memory")
; #define PG8_BAR __builtin_amdgcn_s_barrier()
; #define PG8_SCHED __builtin_amdgcn_sched_barrier(0)
; template <class Epi, class Sched, bool ALIGN_EPI = false, bool SP2 = false, bool FP8 = false>
; __device__ __forceinline__ void gemm_phase(LAS unsigned char* lds, const Gemm g, const Sched& S, const Epi& E, int wbase) {
;     ...
;             PG8_LDB(B0, 1, 0); PG8_LDB(B1, 1, 1); PG8_SCHED; PG8_LDA(At, 1, 0); PG8_STAGE(PG8_SA(0, 1), rA2, a2 + hstep, voffA);
;             PG8_WAIT_V(8); PG8_WAIT_L(0); PG8_BAR; PG8_MMA(0, 0, At, B0); PG8_MMA(0, 1, At, B1); PG8_BAR; PG8_SCHED;
;             PG8_LDA(At, 1, 1); PG8_STAGE(PG8_SB(1, 0), rB2, b3, voffB); PG8_STAGE(PG8_SB(1, 1), rB2, b3 + hstep, voffB); PG8_STAGE(PG8_SA(1, 0), rA2, a3, voffA);
;             PG8_WAIT_V(8); PG8_WAIT_L(0); PG8_BAR; PG8_MMA(1, 0, At, B0); PG8_MMA(1, 1, At, B1); PG8_BAR; PG8_SCHED;
	v_add_u32_e32 v8, 0x18000, v180
	s_nop 3
	ds_read_b128 v[0:3], v8
	ds_read_b128 v[4:7], v8 offset:1024
	ds_read_b128 v[16:19], v8 offset:2048
	ds_read_b128 v[20:23], v8 offset:3072
	v_add_u32_e32 v8, 0x1c000, v180
	ds_read_b128 v[120:123], v8
	ds_read_b128 v[124:127], v8 offset:1024
	ds_read_b128 v[132:135], v8 offset:2048
	ds_read_b128 v[136:139], v8 offset:3072
	s_add_i32 s62, s62, s42
	s_mov_b32 m0, s52
	ds_read_b128 v[8:11], v181 offset:32768
	ds_read_b128 v[12:15], v181 offset:33792
	ds_read_b128 v[24:27], v181 offset:34816
	ds_read_b128 v[28:31], v181 offset:35840
	ds_read_b128 v[32:35], v181 offset:36864
	ds_read_b128 v[36:39], v181 offset:37888
	ds_read_b128 v[40:43], v181 offset:38912
	ds_read_b128 v[44:47], v181 offset:39936
	buffer_load_dwordx4 v174, s[36:39], s62 offen lds
	s_mov_b32 m0, s53
	s_nop 0
	buffer_load_dwordx4 v176, s[36:39], s62 offen lds
	s_waitcnt vmcnt(8)
	s_waitcnt lgkmcnt(0)
	s_barrier
	s_setprio 1
	s_waitcnt lgkmcnt(6)
	v_mfma_f32_16x16x128_f8f6f4 v[140:143], v[0:7], v[8:15], v[140:143]
	v_mfma_f32_16x16x128_f8f6f4 v[128:131], v[16:23], v[8:15], v[128:131]
	s_waitcnt lgkmcnt(4)
	v_mfma_f32_16x16x128_f8f6f4 v[108:111], v[0:7], v[24:31], v[108:111]
	v_mfma_f32_16x16x128_f8f6f4 v[104:107], v[16:23], v[24:31], v[104:107]
	s_waitcnt lgkmcnt(2)
	v_mfma_f32_16x16x128_f8f6f4 v[92:95], v[0:7], v[32:39], v[168:171]
	v_mfma_f32_16x16x128_f8f6f4 v[88:91], v[16:23], v[32:39], v[190:193]
	s_waitcnt lgkmcnt(0)
	v_mfma_f32_16x16x128_f8f6f4 v[76:79], v[0:7], v[40:47], v[210:213]
	v_mfma_f32_16x16x128_f8f6f4 v[72:75], v[16:23], v[40:47], v[214:217]
	s_setprio 0
	s_setprio 1
	v_mfma_f32_16x16x128_f8f6f4 v[116:119], v[120:127], v[8:15], v[116:119]
	v_mfma_f32_16x16x128_f8f6f4 v[112:115], v[132:139], v[8:15], v[112:115]
	v_mfma_f32_16x16x128_f8f6f4 v[100:103], v[120:127], v[24:31], v[100:103]
	v_mfma_f32_16x16x128_f8f6f4 v[96:99], v[132:139], v[24:31], v[96:99]
	v_mfma_f32_16x16x128_f8f6f4 v[84:87], v[120:127], v[32:39], v[160:163]
	v_mfma_f32_16x16x128_f8f6f4 v[80:83], v[132:139], v[32:39], v[164:167]
	v_mfma_f32_16x16x128_f8f6f4 v[68:71], v[120:127], v[40:47], v[182:185]
	v_mfma_f32_16x16x128_f8f6f4 v[64:67], v[132:139], v[40:47], v[186:189]
	s_setprio 0
	s_barrier
	s_mov_b32 m0, s56
	s_bitset1_b32 s55, 7
	ds_read_b128 v[32:35], v181 offset:49152
	ds_read_b128 v[36:39], v181 offset:50176
	ds_read_b128 v[144:147], v181 offset:51200
	ds_read_b128 v[148:151], v181 offset:52224
	ds_read_b128 v[152:155], v181 offset:53248
	ds_read_b128 v[156:159], v181 offset:54272
	ds_read_b128 v[160:163], v181 offset:55296
	ds_read_b128 v[164:167], v181 offset:56320
	buffer_load_dwordx4 v175, s[12:15], s55 offen lds
	s_mov_b32 m0, s57
	s_nop 0
	buffer_load_dwordx4 v177, s[12:15], s55 offen lds
	s_add_i32 s55, s55, s42
	s_mov_b32 m0, s65
	s_nop 0
	buffer_load_dwordx4 v175, s[12:15], s55 offen lds
	s_mov_b32 m0, s76
	s_nop 0
	buffer_load_dwordx4 v177, s[12:15], s55 offen lds
	s_mov_b32 m0, s58
	s_nop 0
	buffer_load_dwordx4 v174, s[36:39], s54 offen lds
	s_mov_b32 m0, s59
	s_nop 0
	buffer_load_dwordx4 v176, s[36:39], s54 offen lds
	s_waitcnt vmcnt(8)
	s_waitcnt lgkmcnt(0)
	s_barrier
	s_setprio 1
	s_waitcnt lgkmcnt(6)
	v_mfma_f32_16x16x128_f8f6f4 v[60:63], v[0:7], v[32:39], v[60:63]
	v_mfma_f32_16x16x128_f8f6f4 v[56:59], v[16:23], v[32:39], v[56:59]
	s_waitcnt lgkmcnt(4)
	v_mfma_f32_16x16x128_f8f6f4 v[44:47], v[0:7], v[144:151], v[194:197]
	v_mfma_f32_16x16x128_f8f6f4 v[40:43], v[16:23], v[144:151], v[198:201]
	s_waitcnt lgkmcnt(2)
	v_mfma_f32_16x16x128_f8f6f4 v[28:31], v[0:7], v[152:159], v[202:205]
	v_mfma_f32_16x16x128_f8f6f4 v[24:27], v[16:23], v[152:159], v[206:209]
	s_waitcnt lgkmcnt(0)
	v_mfma_f32_16x16x128_f8f6f4 v[12:15], v[0:7], v[160:167], v[218:221]
	v_mfma_f32_16x16x128_f8f6f4 v[8:11], v[16:23], v[160:167], v[226:229]
	s_setprio 0
	s_setprio 1
	v_mfma_f32_16x16x128_f8f6f4 v[52:55], v[120:127], v[32:39], v[52:55]
	v_mfma_f32_16x16x128_f8f6f4 v[48:51], v[132:139], v[32:39], v[48:51]
	v_mfma_f32_16x16x128_f8f6f4 v[36:39], v[120:127], v[144:151], v[230:233]
	v_mfma_f32_16x16x128_f8f6f4 v[32:35], v[132:139], v[144:151], v[234:237]
	v_mfma_f32_16x16x128_f8f6f4 v[20:23], v[120:127], v[152:159], v[238:241]
	v_mfma_f32_16x16x128_f8f6f4 v[16:19], v[132:139], v[152:159], v[242:245]
	v_mfma_f32_16x16x128_f8f6f4 v[4:7], v[120:127], v[160:167], v[246:249]
	v_mfma_f32_16x16x128_f8f6f4 v[0:3], v[132:139], v[160:167], v[250:253]
	s_setprio 0
	s_barrier
	s_add_i32 s61, s61, 2
	s_addk_i32 s4, 0x100
	s_addk_i32 s5, 0x100
	s_cmp_ge_i32 s61, s82
	s_cbranch_scc0 .LBB0_1990
	v_mov_b32_e32 v230, v172
	v_mov_b32_e32 v233, v173
	v_mov_b32_e32 v231, v222
	v_mov_b32_e32 v234, v223
	s_and_b64 vcc, exec, s[28:29]
	s_cbranch_vccnz .LBB0_1993
	s_branch .LBB0_1994
